# MoE fp8 GEMMs: weight-tile LDS-DMA source rows remapped so a lane's 16 columns are consecutive; epilogue stores merged (P9 2xdword->dwordx2, P10 2xdwordx2->dwordx4)
# speedup vs baseline: 1.0150x; 1.0124x over previous
.LBB0_1147:
	s_add_u32 s4, s92, 0x50ee1c00
	s_addc_u32 s5, s93, 0
	s_add_u32 s8, s92, 0x38ee1c00
	s_addc_u32 s3, s93, 0
	s_add_u32 s12, s92, 0x176e1c00
	s_addc_u32 s13, s93, 0
	s_lshl_b32 s2, s86, 10
	v_lshl_or_b32 v0, v133, 4, s2
	v_ashrrev_i32_e32 v1, 31, v0
	v_lshrrev_b32_e32 v1, 22, v1
	v_add_u32_e32 v1, v0, v1
	v_ashrrev_i32_e32 v132, 10, v1
	v_mul_i32_i24_e32 v1, 0x400, v132
	v_sub_u32_e32 v1, v0, v1
	v_lshrrev_b32_e32 v2, 4, v1
	v_bitop3_b32 v138, v2, v1, 32 bitop3:0x6c
	v_ashrrev_i32_e32 v2, 31, v138
	v_lshrrev_b32_e32 v2, 26, v2
	v_lshlrev_b32_e32 v1, 3, v132
	v_add_u32_e32 v139, v138, v2
	v_and_b32_e32 v1, -16, v1
	v_ashrrev_i32_e32 v140, 6, v139
	v_add_u32_e32 v0, 0x2000, v0
	v_add_u32_e32 v152, v140, v1
	v_ashrrev_i32_e32 v1, 31, v0
	v_lshrrev_b32_e32 v1, 22, v1
	v_add_u32_e32 v1, v0, v1
	v_ashrrev_i32_e32 v141, 10, v1
	v_mul_i32_i24_e32 v1, 0x400, v141
	v_sub_u32_e32 v0, v0, v1
	v_lshrrev_b32_e32 v1, 4, v0
	v_bitop3_b32 v142, v1, v0, 32 bitop3:0x6c
	v_ashrrev_i32_e32 v1, 31, v142
	v_ashrrev_i32_e32 v129, 31, v128
	v_lshrrev_b32_e32 v1, 26, v1
	s_add_i32 s9, s38, -1
	v_lshlrev_b64 v[134:135], 18, v[128:129]
	v_lshlrev_b32_e32 v0, 3, v141
	v_add_u32_e32 v143, v142, v1
	v_min_i32_e32 v130, s9, v152
	v_lshl_add_u64 v[134:135], s[12:13], 0, v[134:135]
	s_lshl_b64 s[6:7], s[6:7], 2
	v_and_b32_e32 v0, -16, v0
	v_ashrrev_i32_e32 v144, 6, v143
	v_ashrrev_i32_e32 v131, 31, v130
	v_lshl_add_u64 v[134:135], v[134:135], 0, s[6:7]
	v_add_u32_e32 v153, v144, v0
	v_lshl_add_u64 v[130:131], v[130:131], 2, v[134:135]
	v_add_u32_e32 v154, 0x80, v152
	v_mov_b64 v[124:125], 0
	v_mov_b64 v[126:127], 0
	v_mov_b64 v[120:121], 0
	v_mov_b64 v[122:123], 0
	v_mov_b64 v[108:109], 0
	v_mov_b64 v[110:111], 0
	v_mov_b64 v[104:105], 0
	v_mov_b64 v[106:107], 0
	v_mov_b64 v[92:93], 0
	v_mov_b64 v[94:95], 0
	v_mov_b64 v[88:89], 0
	v_mov_b64 v[90:91], 0
	v_mov_b64 v[76:77], 0
	v_mov_b64 v[78:79], 0
	v_mov_b64 v[72:73], 0
	v_mov_b64 v[74:75], 0
	v_mov_b64 v[116:117], 0
	v_mov_b64 v[118:119], 0
	v_mov_b64 v[112:113], 0
	v_mov_b64 v[114:115], 0
	v_mov_b64 v[100:101], 0
	v_mov_b64 v[102:103], 0
	v_mov_b64 v[96:97], 0
	v_mov_b64 v[98:99], 0
	v_mov_b64 v[84:85], 0
	v_mov_b64 v[86:87], 0
	v_mov_b64 v[80:81], 0
	v_mov_b64 v[82:83], 0
	v_mov_b64 v[68:69], 0
	v_mov_b64 v[70:71], 0
	v_mov_b64 v[64:65], 0
	v_mov_b64 v[66:67], 0
	s_waitcnt vmcnt(7)
	v_mov_b64 v[60:61], 0
	v_mov_b64 v[62:63], 0
	s_waitcnt vmcnt(4)
	v_mov_b64 v[56:57], 0
	v_mov_b64 v[58:59], 0
	v_mov_b64 v[44:45], 0
	v_mov_b64 v[46:47], 0
	v_mov_b64 v[40:41], 0
	v_mov_b64 v[42:43], 0
	v_mov_b64 v[28:29], 0
	v_mov_b64 v[30:31], 0
	v_mov_b64 v[24:25], 0
	v_mov_b64 v[26:27], 0
	v_mov_b64 v[12:13], 0
	v_mov_b64 v[14:15], 0
	v_mov_b64 v[8:9], 0
	v_mov_b64 v[10:11], 0
	v_mov_b64 v[52:53], 0
	v_mov_b64 v[54:55], 0
	v_mov_b64 v[48:49], 0
	v_mov_b64 v[50:51], 0
	v_mov_b64 v[36:37], 0
	v_mov_b64 v[38:39], 0
	v_mov_b64 v[32:33], 0
	v_mov_b64 v[34:35], 0
	v_mov_b64 v[20:21], 0
	v_mov_b64 v[22:23], 0
	v_mov_b64 v[16:17], 0
	v_mov_b64 v[18:19], 0
	v_mov_b64 v[4:5], 0
	v_mov_b64 v[6:7], 0
	v_mov_b64 v[0:1], 0
	v_mov_b64 v[2:3], 0
	global_load_dword v129, v[130:131], off
	v_min_i32_e32 v130, s9, v153
	v_min_i32_e32 v136, s9, v154
	v_ashrrev_i32_e32 v131, 31, v130
	v_ashrrev_i32_e32 v137, 31, v136
	v_lshl_add_u64 v[130:131], v[130:131], 2, v[134:135]
	v_lshl_add_u64 v[136:137], v[136:137], 2, v[134:135]
	v_add_u32_e32 v155, 0x80, v153
	global_load_dword v145, v[130:131], off
	s_nop 0
	global_load_dword v136, v[136:137], off
	v_min_i32_e32 v130, s9, v155
	v_ashrrev_i32_e32 v131, 31, v130
	v_lshl_add_u64 v[130:131], v[130:131], 2, v[134:135]
	global_load_dword v134, v[130:131], off
	v_and_b32_e32 v131, 0xc0, v139
	v_lshlrev_b32_e32 v130, 5, v132
	v_sub_u32_e32 v131, v138, v131
	v_mov_b32_e32 v132, 1
	v_and_b32_e32 v130, 32, v130
	v_ashrrev_i16_sdwa v131, v132, sext(v131) dst_sel:DWORD dst_unused:UNUSED_PAD src0_sel:DWORD src1_sel:BYTE_0
	v_add_u32_sdwa v156, v130, sext(v131) dst_sel:DWORD dst_unused:UNUSED_PAD src0_sel:DWORD src1_sel:WORD_0
	v_lshlrev_b32_e32 v130, 1, v152
	v_lshrrev_b32_e32 v131, 2, v152
	v_and_b32_e32 v135, 3, v140
	s_mov_b32 s6, 0x1fffe0
	v_and_b32_e32 v130, 24, v130
	v_and_b32_e32 v131, 4, v131
	v_and_or_b32 v135, v152, s6, v135
	v_or3_b32 v130, v135, v131, v130
	v_lshlrev_b32_e32 v131, 1, v156
	v_lshl_add_u32 v157, v130, 11, v131
	v_and_b32_e32 v200, 0x3c000, v157
	v_add_u32_e32 v157, v157, v200
	v_and_b32_e32 v131, 0xffc0, v143
	v_sub_u32_e32 v131, v142, v131
	v_lshrrev_b16_e32 v135, 7, v131
	v_and_b32_e32 v135, 1, v135
	v_lshlrev_b32_e32 v130, 5, v141
	v_add_u16_e32 v131, v131, v135
	v_and_b32_e32 v130, 32, v130
	v_ashrrev_i16_sdwa v131, v132, sext(v131) dst_sel:DWORD dst_unused:UNUSED_PAD src0_sel:DWORD src1_sel:BYTE_0
	v_add_u32_sdwa v158, v130, sext(v131) dst_sel:DWORD dst_unused:UNUSED_PAD src0_sel:DWORD src1_sel:WORD_0
	v_lshlrev_b32_e32 v130, 1, v153
	v_lshrrev_b32_e32 v131, 2, v153
	v_and_b32_e32 v132, 3, v144
	v_and_b32_e32 v130, 24, v130
	v_and_b32_e32 v131, 4, v131
	v_and_or_b32 v132, v153, s6, v132
	v_or3_b32 v130, v132, v131, v130
	s_and_b32 s9, s3, 0xffff
	s_lshl_b32 s3, s65, 18
	s_add_i32 s25, s2, 0
	s_mov_b32 s7, 0x20000
	s_mov_b32 s6, -1
	s_add_i32 s26, s25, 0x10000
	v_lshlrev_b32_e32 v131, 1, v158
	s_mov_b32 s10, s6
	s_mov_b32 s11, s7
	s_mov_b32 m0, s26
	s_add_i32 s27, s25, 0x12000
	v_lshl_add_u32 v159, v130, 11, v131
	v_and_b32_e32 v200, 0x3c000, v159
	v_add_u32_e32 v159, v159, v200
	s_add_i32 s28, s25, 0x14000
	s_add_i32 s29, s25, 0x16000
	s_and_b32 s5, s5, 0xffff
	s_add_i32 s30, s25, 0x2000
	s_add_i32 s31, s25, 0x4000
	s_add_i32 s33, s25, 0x6000
	s_mov_b32 s34, 0
	s_waitcnt vmcnt(3)
	v_lshlrev_b32_e32 v129, 8, v129
	v_and_b32_e32 v129, 0x7ffffc00, v129
	v_add_lshl_u32 v129, v129, v156, 1
	s_waitcnt vmcnt(2)
	v_lshlrev_b32_e32 v130, 8, v145
	v_and_b32_e32 v130, 0x7ffffc00, v130
	s_waitcnt vmcnt(1)
	v_lshlrev_b32_e32 v131, 8, v136
	v_add_lshl_u32 v130, v130, v158, 1
	v_and_b32_e32 v131, 0x7ffffc00, v131
	s_waitcnt vmcnt(0)
	v_lshlrev_b32_e32 v132, 8, v134
	v_lshlrev_b32_e32 v134, 22, v128
	v_add_u32_e32 v134, s3, v134
	v_add_lshl_u32 v131, v131, v156, 1
	v_readfirstlane_b32 s3, v134
	s_lshl_b32 s66, s3, 1
	buffer_load_dwordx4 v157, s[8:11], s66 offen lds
	s_mov_b32 m0, s27
	s_add_i32 s2, s66, 0x4000
	buffer_load_dwordx4 v159, s[8:11], s66 offen lds
	s_mov_b32 m0, s28
	v_and_b32_e32 v132, 0x7ffffc00, v132
	buffer_load_dwordx4 v157, s[8:11], s2 offen lds
	s_mov_b32 m0, s29
	v_add_lshl_u32 v132, v132, v158, 1
	buffer_load_dwordx4 v159, s[8:11], s2 offen lds
	s_mov_b32 m0, s25
	s_lshr_b32 s2, s90, 8
	buffer_load_dwordx4 v129, s[4:7], 0 offen lds
	s_mov_b32 m0, s30
	s_cmp_eq_u32 s2, 1
	buffer_load_dwordx4 v130, s[4:7], 0 offen lds
	s_mov_b32 m0, s31
	s_movk_i32 s3, 0x80
	buffer_load_dwordx4 v131, s[4:7], 0 offen lds
	s_mov_b32 m0, s33
	s_cselect_b64 s[14:15], -1, 0
	buffer_load_dwordx4 v132, s[4:7], 0 offen lds
	s_cmp_lg_u32 s2, 1
	s_cbranch_scc1 .LBB0_1149
	s_barrier
.LBB0_1149:
	s_add_u32 s16, s92, 0x52ee1c00
	s_addc_u32 s17, s93, 0
	s_add_i32 s35, s25, 0x18000
	s_add_i32 s18, s66, 0x80
	s_mov_b32 s10, s6
	s_mov_b32 s11, s7
	s_mov_b32 m0, s35
	s_add_i32 s36, s25, 0x1a000
	s_waitcnt vmcnt(2)
	s_barrier
	buffer_load_dwordx4 v157, s[8:11], s18 offen lds
	s_mov_b32 m0, s36
	s_add_i32 s37, s25, 0x8000
	buffer_load_dwordx4 v159, s[8:11], s18 offen lds
	s_mov_b32 m0, s37
	s_add_i32 s40, s25, 0xa000
	buffer_load_dwordx4 v129, s[4:7], s3 offen lds
	s_mov_b32 m0, s40
	s_add_i32 s41, s25, 0x1c000
	buffer_load_dwordx4 v130, s[4:7], s3 offen lds
	s_add_i32 s3, s66, 0x4080
	s_mov_b32 m0, s41
	s_add_i32 s42, s25, 0x1e000
	buffer_load_dwordx4 v157, s[8:11], s3 offen lds
	s_mov_b32 m0, s42
	v_and_b32_e32 v134, 15, v133
	buffer_load_dwordx4 v159, s[8:11], s3 offen lds
	v_lshrrev_b32_e32 v135, 1, v133
	v_lshrrev_b32_e32 v136, 6, v133
	v_and_b32_e32 v137, 48, v133
	v_lshlrev_b32_e32 v133, 2, v133
	v_lshlrev_b32_e32 v139, 6, v134
	v_and_b32_e32 v133, 32, v133
	s_lshl_b32 s3, s2, 6
	s_lshl_b32 s2, s2, 13
	v_lshlrev_b32_e32 v138, 10, v136
	v_bitop3_b32 v140, v139, v133, v137 bitop3:0x36
	v_or3_b32 v138, v138, s2, v140
	s_lshl_b32 s2, s86, 5
	s_and_b32 s2, s2, 0x60
	s_lshr_b32 s10, s2, 3
	s_add_i32 s43, s25, 0xc000
	s_add_i32 s44, s25, 0xe000
	v_or_b32_e32 v136, s10, v136
	s_cmpk_lt_u32 s90, 0x100
	v_or_b32_e32 v160, s3, v134
	v_or_b32_e32 v137, v139, v137
	v_lshlrev_b32_e32 v136, 10, v136
	s_waitcnt vmcnt(6)
	s_cselect_b64 s[18:19], -1, 0
	s_addk_i32 s3, 0x80
	v_and_b32_e32 v135, 56, v135
	v_bitop3_b32 v133, v137, v136, v133 bitop3:0xde
	v_or_b32_e32 v165, s3, v134
	v_add_u32_e32 v161, s2, v135
	v_lshlrev_b32_e32 v161, 1, v161
	v_or_b32_e32 v162, 16, v160
	v_or_b32_e32 v163, 32, v160
	v_or_b32_e32 v164, 48, v160
	v_or_b32_e32 v166, 16, v165
	v_or_b32_e32 v167, 32, v165
	v_or_b32_e32 v168, 48, v165
	s_add_i32 s45, 0, 0x20084
	s_add_i32 s46, 0, 0x2008c
	s_add_i32 s47, 0, 0x20094
	s_add_i32 s48, 0, 0x2009c
	s_add_i32 s49, 0, 0x200a4
	s_add_i32 s50, 0, 0x200ac
	s_add_i32 s51, 0, 0x200b4
	s_add_i32 s52, 0, 0x200bc
	s_add_i32 s53, 0, 0x200c4
	s_add_i32 s54, 0, 0x200cc
	s_add_i32 s55, 0, 0x200d4
	s_add_i32 s56, 0, 0x200dc
	s_add_i32 s57, 0, 0x200e4
	s_add_i32 s58, 0, 0x200ec
	s_add_i32 s59, 0, 0x200f4
	s_add_i32 s60, 0, 0x200fc
	v_add_u32_e32 v169, 0, v133
	v_add_u32_e32 v170, 0, v138
	v_mov_b32_e32 v171, 0x7f7f7f7f
	v_mov_b32_e32 v145, 0
	s_mov_b32 s20, 0x3c800000
	s_mov_b32 s61, 0xc0e00000
	v_mov_b32_e32 v172, 0x40e00000
	s_barrier
	s_branch .LBB0_1152

.LBB0_1156:
	v_mov_b32_e32 v248, v128
	v_ashrrev_i32_e32 v249, 31, v128
	v_lshl_or_b32 v250, s65, 8, v161
	v_lshlrev_b64 v[248:249], 14, v[248:249]
	v_ashrrev_i32_e32 v251, 31, v250
	v_lshl_add_u64 v[248:249], s[72:73], 0, v[248:249]
	v_lshl_add_u64 v[248:249], v[250:251], 2, v[248:249]
	global_load_dwordx4 v[232:235], v[248:249], off
	global_load_dwordx4 v[236:239], v[248:249], off offset:16
	global_load_dwordx4 v[240:243], v[248:249], off offset:32
	global_load_dwordx4 v[244:247], v[248:249], off offset:48
	s_mov_b32 s67, -2
	s_movk_i32 s68, 0x100

.Lp9_na_done:
	v_add_u32_e32 v133, 0x10000, v169
	v_add_u32_e32 v142, 0x14000, v169
	ds_read_b128 v[134:137], v133
	ds_read_b128 v[138:141], v133 offset:1024
	ds_read_b128 v[176:179], v133 offset:2048
	ds_read_b128 v[180:183], v133 offset:3072
	ds_read_b128 v[184:187], v142
	ds_read_b128 v[188:191], v142 offset:1024
	ds_read_b128 v[192:195], v142 offset:2048
	ds_read_b128 v[196:199], v142 offset:3072
	s_add_i32 s70, s66, s68
	s_add_i32 s71, s68, 0xffffff80
	s_cmp_eq_u32 s67, 12
	s_cselect_b64 vcc, -1, 0
	s_and_b64 s[10:11], vcc, exec
	v_cndmask_b32_e32 v133, v129, v147, vcc
	s_cselect_b32 s69, 0, s68
	v_cndmask_b32_e32 v142, v131, v174, vcc
	v_cndmask_b32_e32 v143, v130, v173, vcc
	s_mov_b32 m0, s43
	ds_read_b128 v[200:203], v170
	ds_read_b128 v[204:207], v170 offset:1024
	ds_read_b128 v[208:211], v170 offset:2048
	ds_read_b128 v[212:215], v170 offset:3072
	ds_read_b128 v[216:219], v170 offset:4096
	ds_read_b128 v[220:223], v170 offset:5120
	ds_read_b128 v[224:227], v170 offset:6144
	ds_read_b128 v[228:231], v170 offset:7168
	buffer_load_dwordx4 v131, s[4:7], s71 offen lds
	s_mov_b32 m0, s44
	s_cselect_b32 s70, s23, s70
	buffer_load_dwordx4 v132, s[4:7], s71 offen lds
	s_waitcnt vmcnt(8)
	s_waitcnt lgkmcnt(0)
	s_barrier
	s_setprio 1
	s_nop 1
	s_waitcnt lgkmcnt(6)
	v_mfma_f32_16x16x128_f8f6f4 v[124:127], v[134:141], v[200:207], v[124:127]
	v_mfma_f32_16x16x128_f8f6f4 v[120:123], v[176:183], v[200:207], v[120:123]
	s_waitcnt lgkmcnt(4)
	v_mfma_f32_16x16x128_f8f6f4 v[108:111], v[134:141], v[208:215], v[108:111]
	v_mfma_f32_16x16x128_f8f6f4 v[104:107], v[176:183], v[208:215], v[104:107]
	s_waitcnt lgkmcnt(2)
	v_mfma_f32_16x16x128_f8f6f4 v[92:95], v[134:141], v[216:223], v[92:95]
	v_mfma_f32_16x16x128_f8f6f4 v[88:91], v[176:183], v[216:223], v[88:91]
	s_waitcnt lgkmcnt(0)
	v_mfma_f32_16x16x128_f8f6f4 v[76:79], v[134:141], v[224:231], v[76:79]
	v_mfma_f32_16x16x128_f8f6f4 v[72:75], v[176:183], v[224:231], v[72:75]
	s_setprio 0
	s_setprio 1
	s_nop 1
	v_mfma_f32_16x16x128_f8f6f4 v[116:119], v[184:191], v[200:207], v[116:119]
	v_mfma_f32_16x16x128_f8f6f4 v[112:115], v[192:199], v[200:207], v[112:115]
	v_mfma_f32_16x16x128_f8f6f4 v[100:103], v[184:191], v[208:215], v[100:103]
	v_mfma_f32_16x16x128_f8f6f4 v[96:99], v[192:199], v[208:215], v[96:99]
	v_mfma_f32_16x16x128_f8f6f4 v[84:87], v[184:191], v[216:223], v[84:87]
	v_mfma_f32_16x16x128_f8f6f4 v[80:83], v[192:199], v[216:223], v[80:83]
	v_mfma_f32_16x16x128_f8f6f4 v[68:71], v[184:191], v[224:231], v[68:71]
	v_mfma_f32_16x16x128_f8f6f4 v[64:67], v[192:199], v[224:231], v[64:67]
	s_setprio 0
	s_barrier
	s_mov_b32 m0, s26
	s_mov_b32 s10, s6
	s_mov_b32 s11, s7
	ds_read_b128 v[200:203], v170 offset:16384
	ds_read_b128 v[204:207], v170 offset:17408
	ds_read_b128 v[208:211], v170 offset:18432
	ds_read_b128 v[212:215], v170 offset:19456
	ds_read_b128 v[216:219], v170 offset:20480
	ds_read_b128 v[220:223], v170 offset:21504
	ds_read_b128 v[224:227], v170 offset:22528
	ds_read_b128 v[228:231], v170 offset:23552
	buffer_load_dwordx4 v157, s[8:11], s70 offen lds
	s_mov_b32 m0, s27
	s_add_i32 s71, s70, 0x4000
	buffer_load_dwordx4 v159, s[8:11], s70 offen lds
	s_mov_b32 m0, s28
	s_nop 0
	buffer_load_dwordx4 v157, s[8:11], s71 offen lds
	s_mov_b32 m0, s29
	s_nop 0
	buffer_load_dwordx4 v159, s[8:11], s71 offen lds
	s_mov_b32 m0, s25
	s_nop 0
	buffer_load_dwordx4 v133, s[4:7], s69 offen lds
	s_mov_b32 m0, s30
	s_nop 0
	buffer_load_dwordx4 v143, s[4:7], s69 offen lds
	s_waitcnt vmcnt(8)
	s_waitcnt lgkmcnt(0)
	s_barrier
	s_setprio 1
	s_nop 1
	s_waitcnt lgkmcnt(6)
	v_mfma_f32_16x16x128_f8f6f4 v[60:63], v[134:141], v[200:207], v[60:63]
	v_mfma_f32_16x16x128_f8f6f4 v[56:59], v[176:183], v[200:207], v[56:59]
	s_waitcnt lgkmcnt(4)
	v_mfma_f32_16x16x128_f8f6f4 v[44:47], v[134:141], v[208:215], v[44:47]
	v_mfma_f32_16x16x128_f8f6f4 v[40:43], v[176:183], v[208:215], v[40:43]
	s_waitcnt lgkmcnt(2)
	v_mfma_f32_16x16x128_f8f6f4 v[28:31], v[134:141], v[216:223], v[28:31]
	v_mfma_f32_16x16x128_f8f6f4 v[24:27], v[176:183], v[216:223], v[24:27]
	s_waitcnt lgkmcnt(0)
	v_mfma_f32_16x16x128_f8f6f4 v[12:15], v[134:141], v[224:231], v[12:15]
	v_mfma_f32_16x16x128_f8f6f4 v[8:11], v[176:183], v[224:231], v[8:11]
	s_setprio 0
	s_setprio 1
	s_nop 1
	v_mfma_f32_16x16x128_f8f6f4 v[52:55], v[184:191], v[200:207], v[52:55]
	v_mfma_f32_16x16x128_f8f6f4 v[48:51], v[192:199], v[200:207], v[48:51]
	v_mfma_f32_16x16x128_f8f6f4 v[36:39], v[184:191], v[208:215], v[36:39]
	v_mfma_f32_16x16x128_f8f6f4 v[32:35], v[192:199], v[208:215], v[32:35]
	v_mfma_f32_16x16x128_f8f6f4 v[20:23], v[184:191], v[216:223], v[20:23]
	v_mfma_f32_16x16x128_f8f6f4 v[16:19], v[192:199], v[216:223], v[16:19]
	v_mfma_f32_16x16x128_f8f6f4 v[4:7], v[184:191], v[224:231], v[4:7]
	v_mfma_f32_16x16x128_f8f6f4 v[0:3], v[192:199], v[224:231], v[0:3]
	s_setprio 0
	s_barrier
	v_add_u32_e32 v144, 0x18000, v169
	ds_read_b128 v[134:137], v144
	ds_read_b128 v[138:141], v144 offset:1024
	ds_read_b128 v[176:179], v144 offset:2048
	ds_read_b128 v[180:183], v144 offset:3072
	v_add_u32_e32 v144, 0x1c000, v169
	ds_read_b128 v[184:187], v144
	ds_read_b128 v[188:191], v144 offset:1024
	ds_read_b128 v[192:195], v144 offset:2048
	ds_read_b128 v[196:199], v144 offset:3072
	s_mov_b32 m0, s31
	ds_read_b128 v[200:203], v170 offset:32768
	ds_read_b128 v[204:207], v170 offset:33792
	ds_read_b128 v[208:211], v170 offset:34816
	ds_read_b128 v[212:215], v170 offset:35840
	ds_read_b128 v[216:219], v170 offset:36864
	ds_read_b128 v[220:223], v170 offset:37888
	ds_read_b128 v[224:227], v170 offset:38912
	ds_read_b128 v[228:231], v170 offset:39936
	v_cndmask_b32_e32 v144, v132, v175, vcc
	buffer_load_dwordx4 v142, s[4:7], s69 offen lds
	s_mov_b32 m0, s33
	s_nop 0
	buffer_load_dwordx4 v144, s[4:7], s69 offen lds
	s_waitcnt vmcnt(8)
	s_waitcnt lgkmcnt(0)
	s_barrier
	s_setprio 1
	s_nop 1
	s_waitcnt lgkmcnt(6)
	v_mfma_f32_16x16x128_f8f6f4 v[124:127], v[134:141], v[200:207], v[124:127]
	v_mfma_f32_16x16x128_f8f6f4 v[120:123], v[176:183], v[200:207], v[120:123]
	s_waitcnt lgkmcnt(4)
	v_mfma_f32_16x16x128_f8f6f4 v[108:111], v[134:141], v[208:215], v[108:111]
	v_mfma_f32_16x16x128_f8f6f4 v[104:107], v[176:183], v[208:215], v[104:107]
	s_waitcnt lgkmcnt(2)
	v_mfma_f32_16x16x128_f8f6f4 v[92:95], v[134:141], v[216:223], v[92:95]
	v_mfma_f32_16x16x128_f8f6f4 v[88:91], v[176:183], v[216:223], v[88:91]
	s_waitcnt lgkmcnt(0)
	v_mfma_f32_16x16x128_f8f6f4 v[76:79], v[134:141], v[224:231], v[76:79]
	v_mfma_f32_16x16x128_f8f6f4 v[72:75], v[176:183], v[224:231], v[72:75]
	s_setprio 0
	s_setprio 1
	s_nop 1
	v_mfma_f32_16x16x128_f8f6f4 v[116:119], v[184:191], v[200:207], v[116:119]
	v_mfma_f32_16x16x128_f8f6f4 v[112:115], v[192:199], v[200:207], v[112:115]
	v_mfma_f32_16x16x128_f8f6f4 v[100:103], v[184:191], v[208:215], v[100:103]
	v_mfma_f32_16x16x128_f8f6f4 v[96:99], v[192:199], v[208:215], v[96:99]
	v_mfma_f32_16x16x128_f8f6f4 v[84:87], v[184:191], v[216:223], v[84:87]
	v_mfma_f32_16x16x128_f8f6f4 v[80:83], v[192:199], v[216:223], v[80:83]
	v_mfma_f32_16x16x128_f8f6f4 v[68:71], v[184:191], v[224:231], v[68:71]
	v_mfma_f32_16x16x128_f8f6f4 v[64:67], v[192:199], v[224:231], v[64:67]
	s_setprio 0
	s_barrier
	s_mov_b32 m0, s35
	s_add_i32 s71, s70, 0x80
	ds_read_b128 v[200:203], v170 offset:49152
	ds_read_b128 v[204:207], v170 offset:50176
	ds_read_b128 v[208:211], v170 offset:51200
	ds_read_b128 v[212:215], v170 offset:52224
	ds_read_b128 v[216:219], v170 offset:53248
	ds_read_b128 v[220:223], v170 offset:54272
	ds_read_b128 v[224:227], v170 offset:55296
	ds_read_b128 v[228:231], v170 offset:56320
	buffer_load_dwordx4 v157, s[8:11], s71 offen lds
	s_mov_b32 m0, s36
	s_add_i32 s70, s70, 0x4080
	buffer_load_dwordx4 v159, s[8:11], s71 offen lds
	s_mov_b32 m0, s41
	s_bitset1_b32 s69, 7
	buffer_load_dwordx4 v157, s[8:11], s70 offen lds
	s_mov_b32 m0, s42
	s_nop 0
	buffer_load_dwordx4 v159, s[8:11], s70 offen lds
	s_mov_b32 m0, s37
	s_nop 0
	buffer_load_dwordx4 v133, s[4:7], s69 offen lds
	s_mov_b32 m0, s40
	s_nop 0
	buffer_load_dwordx4 v143, s[4:7], s69 offen lds
	s_waitcnt vmcnt(8)
	s_waitcnt lgkmcnt(0)
	s_barrier
	s_setprio 1
	s_nop 1
	s_waitcnt lgkmcnt(6)
	v_mfma_f32_16x16x128_f8f6f4 v[60:63], v[134:141], v[200:207], v[60:63]
	v_mfma_f32_16x16x128_f8f6f4 v[56:59], v[176:183], v[200:207], v[56:59]
	s_waitcnt lgkmcnt(4)
	v_mfma_f32_16x16x128_f8f6f4 v[44:47], v[134:141], v[208:215], v[44:47]
	v_mfma_f32_16x16x128_f8f6f4 v[40:43], v[176:183], v[208:215], v[40:43]
	s_waitcnt lgkmcnt(2)
	v_mfma_f32_16x16x128_f8f6f4 v[28:31], v[134:141], v[216:223], v[28:31]
	v_mfma_f32_16x16x128_f8f6f4 v[24:27], v[176:183], v[216:223], v[24:27]
	s_waitcnt lgkmcnt(0)
	v_mfma_f32_16x16x128_f8f6f4 v[12:15], v[134:141], v[224:231], v[12:15]
	v_mfma_f32_16x16x128_f8f6f4 v[8:11], v[176:183], v[224:231], v[8:11]
	s_setprio 0
	s_setprio 1
	s_nop 1
	v_mfma_f32_16x16x128_f8f6f4 v[52:55], v[184:191], v[200:207], v[52:55]
	v_mfma_f32_16x16x128_f8f6f4 v[48:51], v[192:199], v[200:207], v[48:51]
	v_mfma_f32_16x16x128_f8f6f4 v[36:39], v[184:191], v[208:215], v[36:39]
	v_mfma_f32_16x16x128_f8f6f4 v[32:35], v[192:199], v[208:215], v[32:35]
	v_mfma_f32_16x16x128_f8f6f4 v[20:23], v[184:191], v[216:223], v[20:23]
	v_mfma_f32_16x16x128_f8f6f4 v[16:19], v[192:199], v[216:223], v[16:19]
	v_mfma_f32_16x16x128_f8f6f4 v[4:7], v[184:191], v[224:231], v[4:7]
	v_mfma_f32_16x16x128_f8f6f4 v[0:3], v[192:199], v[224:231], v[0:3]
	s_setprio 0
	s_barrier
	s_add_i32 s67, s67, 2
	s_addk_i32 s68, 0x100
	s_cmp_gt_u32 s67, 13
	s_cbranch_scc0 .LBB0_1157
	s_and_b64 vcc, exec, s[18:19]
	s_cbranch_vccz .LBB0_1160
	s_barrier
.LBB0_1160:
	v_lshl_or_b32 v148, s65, 8, v161
	v_ashrrev_i32_e32 v149, 31, v148
	s_nop 15
	s_nop 15
	v_add_u32_e32 v144, s39, v160
	v_cmp_gt_i32_e32 vcc, s38, v160
	v_ashrrev_i32_e32 v150, 1, v148
	v_cndmask_b32_e32 v144, -1, v144, vcc
	v_cmp_lt_i32_e32 vcc, -1, v144
	v_ashrrev_i32_e32 v151, 31, v150
	s_and_saveexec_b64 s[10:11], vcc
	s_cbranch_execz .LBB0_1162
	v_pk_fma_f32 v[124:125], v[124:125], s[20:21], v[232:233] op_sel_hi:[1,0,1]
	v_lshlrev_b64 v[176:177], 11, v[144:145]
	v_min_f32_e32 v124, 0x40e00000, v124
	v_mul_f32_e32 v144, 0x3fd9db23, v124
	v_mul_f32_e32 v144, 0xbfb8aa3b, v144
	v_exp_f32_e32 v144, v144
	v_pk_fma_f32 v[126:127], v[126:127], s[20:21], v[234:235] op_sel_hi:[1,0,1]
	v_pk_fma_f32 v[120:121], v[120:121], s[20:21], v[236:237] op_sel_hi:[1,0,1]
	v_min_f32_e32 v126, 0x40e00000, v126
	v_add_f32_e32 v144, 1.0, v144
	v_mul_f32_e32 v149, 0x3fd9db23, v126
	v_rcp_f32_e32 v144, v144
	v_mul_f32_e32 v149, 0xbfb8aa3b, v149
	v_exp_f32_e32 v149, v149
	v_med3_f32 v125, v125, s61, v172
	v_mul_f32_e32 v124, v124, v144
	v_add_f32_e32 v125, 1.0, v125
	v_min_f32_e32 v120, 0x40e00000, v120
	v_add_f32_e32 v144, 1.0, v149
	v_mul_f32_e32 v124, v125, v124
	v_med3_f32 v125, v127, s61, v172
	v_mul_f32_e32 v127, 0x3fd9db23, v120
	v_rcp_f32_e32 v144, v144
	v_mul_f32_e32 v127, 0xbfb8aa3b, v127
	v_exp_f32_e32 v127, v127
	v_pk_fma_f32 v[122:123], v[122:123], s[20:21], v[238:239] op_sel_hi:[1,0,1]
	v_mul_f32_e32 v126, v126, v144
	v_add_f32_e32 v125, 1.0, v125
	v_min_f32_e32 v122, 0x40e00000, v122
	v_mul_f32_e32 v125, v125, v126
	v_add_f32_e32 v126, 1.0, v127
	v_mul_f32_e32 v127, 0x3fd9db23, v122
	v_rcp_f32_e32 v126, v126
	v_mul_f32_e32 v127, 0xbfb8aa3b, v127
	v_exp_f32_e32 v127, v127
	v_med3_f32 v121, v121, s61, v172
	v_mul_f32_e32 v120, v120, v126
	v_add_f32_e32 v121, 1.0, v121
	v_mul_f32_e32 v120, v121, v120
	v_add_f32_e32 v121, 1.0, v127
	v_rcp_f32_e32 v121, v121
	v_cvt_pk_fp8_f32 v200, v124, v125
	v_med3_f32 v123, v123, s61, v172
	v_mul_f32_e32 v121, v122, v121
	v_add_f32_e32 v122, 1.0, v123
	v_pk_fma_f32 v[116:117], v[116:117], s[20:21], v[240:241] op_sel_hi:[1,0,1]
	v_mul_f32_e32 v121, v122, v121
	v_min_f32_e32 v116, 0x40e00000, v116
	v_cvt_pk_fp8_f32 v200, v120, v121 op_sel:[0,0,1]
	v_mul_f32_e32 v120, 0x3fd9db23, v116
	v_mul_f32_e32 v120, 0xbfb8aa3b, v120
	v_exp_f32_e32 v122, v120
	v_pk_fma_f32 v[118:119], v[118:119], s[20:21], v[242:243] op_sel_hi:[1,0,1]
	v_pk_fma_f32 v[112:113], v[112:113], s[20:21], v[244:245] op_sel_hi:[1,0,1]
	v_min_f32_e32 v118, 0x40e00000, v118
	v_add_f32_e32 v122, 1.0, v122
	v_mul_f32_e32 v123, 0x3fd9db23, v118
	v_rcp_f32_e32 v122, v122
	v_mul_f32_e32 v123, 0xbfb8aa3b, v123
	v_exp_f32_e32 v123, v123
	v_med3_f32 v117, v117, s61, v172
	v_mul_f32_e32 v116, v116, v122
	v_add_f32_e32 v117, 1.0, v117
	v_min_f32_e32 v112, 0x40e00000, v112
	v_add_f32_e32 v122, 1.0, v123
	v_mul_f32_e32 v116, v117, v116
	v_med3_f32 v117, v119, s61, v172
	v_mul_f32_e32 v119, 0x3fd9db23, v112
	v_rcp_f32_e32 v122, v122
	v_mul_f32_e32 v119, 0xbfb8aa3b, v119
	v_exp_f32_e32 v119, v119
	v_pk_fma_f32 v[114:115], v[114:115], s[20:21], v[246:247] op_sel_hi:[1,0,1]
	v_mul_f32_e32 v118, v118, v122
	v_add_f32_e32 v117, 1.0, v117
	v_min_f32_e32 v114, 0x40e00000, v114
	v_mul_f32_e32 v117, v117, v118
	v_add_f32_e32 v118, 1.0, v119
	v_mul_f32_e32 v119, 0x3fd9db23, v114
	v_rcp_f32_e32 v118, v118
	v_mul_f32_e32 v119, 0xbfb8aa3b, v119
	v_exp_f32_e32 v119, v119
	v_med3_f32 v113, v113, s61, v172
	v_mul_f32_e32 v112, v112, v118
	v_add_f32_e32 v113, 1.0, v113
	v_mul_f32_e32 v112, v113, v112
	v_add_f32_e32 v113, 1.0, v119
	v_rcp_f32_e32 v113, v113
	v_cvt_pk_fp8_f32 v201, v116, v117
	v_med3_f32 v115, v115, s61, v172
	v_mul_f32_e32 v113, v114, v113
	v_add_f32_e32 v114, 1.0, v115
	v_mul_f32_e32 v113, v114, v113
	v_cvt_pk_fp8_f32 v201, v112, v113 op_sel:[0,0,1]
	v_lshl_add_u64 v[176:177], s[16:17], 0, v[176:177]
	v_lshl_add_u64 v[120:121], v[176:177], 0, v[150:151]
	global_store_dwordx2 v[120:121], v[200:201], off
.LBB0_1162:
	s_or_b64 exec, exec, s[10:11]
	v_add_u32_e32 v112, s39, v162
	v_cmp_gt_i32_e32 vcc, s38, v162
	s_nop 1
	v_cndmask_b32_e32 v144, -1, v112, vcc
	v_cmp_lt_i32_e32 vcc, -1, v144
	s_and_saveexec_b64 s[10:11], vcc
	s_cbranch_execz .LBB0_1164
	v_pk_fma_f32 v[108:109], v[108:109], s[20:21], v[232:233] op_sel_hi:[1,0,1]
	v_pk_fma_f32 v[110:111], v[110:111], s[20:21], v[234:235] op_sel_hi:[1,0,1]
	v_min_f32_e32 v108, 0x40e00000, v108
	v_mul_f32_e32 v114, 0x3fd9db23, v108
	v_mul_f32_e32 v114, 0xbfb8aa3b, v114
	v_exp_f32_e32 v114, v114
	v_min_f32_e32 v110, 0x40e00000, v110
	v_mul_f32_e32 v115, 0x3fd9db23, v110
	v_mul_f32_e32 v115, 0xbfb8aa3b, v115
	v_add_f32_e32 v114, 1.0, v114
	v_rcp_f32_e32 v114, v114
	v_exp_f32_e32 v115, v115
	v_pk_fma_f32 v[104:105], v[104:105], s[20:21], v[236:237] op_sel_hi:[1,0,1]
	v_med3_f32 v109, v109, s61, v172
	v_mul_f32_e32 v108, v108, v114
	v_add_f32_e32 v109, 1.0, v109
	v_min_f32_e32 v104, 0x40e00000, v104
	v_add_f32_e32 v114, 1.0, v115
	v_mul_f32_e32 v108, v109, v108
	v_med3_f32 v109, v111, s61, v172
	v_mul_f32_e32 v111, 0x3fd9db23, v104
	v_rcp_f32_e32 v114, v114
	v_mul_f32_e32 v111, 0xbfb8aa3b, v111
	v_exp_f32_e32 v111, v111
	v_pk_fma_f32 v[106:107], v[106:107], s[20:21], v[238:239] op_sel_hi:[1,0,1]
	v_mul_f32_e32 v110, v110, v114
	v_add_f32_e32 v109, 1.0, v109
	v_min_f32_e32 v106, 0x40e00000, v106
	v_mul_f32_e32 v109, v109, v110
	v_add_f32_e32 v110, 1.0, v111
	v_mul_f32_e32 v111, 0x3fd9db23, v106
	v_rcp_f32_e32 v110, v110
	v_mul_f32_e32 v111, 0xbfb8aa3b, v111
	v_exp_f32_e32 v111, v111
	v_med3_f32 v105, v105, s61, v172
	v_mul_f32_e32 v104, v104, v110
	v_add_f32_e32 v105, 1.0, v105
	v_mul_f32_e32 v104, v105, v104
	v_add_f32_e32 v105, 1.0, v111
	v_rcp_f32_e32 v105, v105
	v_cvt_pk_fp8_f32 v202, v108, v109
	v_med3_f32 v107, v107, s61, v172
	v_mul_f32_e32 v105, v106, v105
	v_add_f32_e32 v106, 1.0, v107
	v_pk_fma_f32 v[100:101], v[100:101], s[20:21], v[240:241] op_sel_hi:[1,0,1]
	v_mul_f32_e32 v105, v106, v105
	v_min_f32_e32 v100, 0x40e00000, v100
	v_cvt_pk_fp8_f32 v202, v104, v105 op_sel:[0,0,1]
	v_mul_f32_e32 v104, 0x3fd9db23, v100
	v_mul_f32_e32 v104, 0xbfb8aa3b, v104
	v_exp_f32_e32 v106, v104
	v_pk_fma_f32 v[102:103], v[102:103], s[20:21], v[242:243] op_sel_hi:[1,0,1]
	v_pk_fma_f32 v[96:97], v[96:97], s[20:21], v[244:245] op_sel_hi:[1,0,1]
	v_min_f32_e32 v102, 0x40e00000, v102
	v_add_f32_e32 v106, 1.0, v106
	v_mul_f32_e32 v107, 0x3fd9db23, v102
	v_rcp_f32_e32 v106, v106
	v_mul_f32_e32 v107, 0xbfb8aa3b, v107
	v_exp_f32_e32 v107, v107
	v_med3_f32 v101, v101, s61, v172
	v_mul_f32_e32 v100, v100, v106
	v_add_f32_e32 v101, 1.0, v101
	v_min_f32_e32 v96, 0x40e00000, v96
	v_add_f32_e32 v106, 1.0, v107
	v_mul_f32_e32 v100, v101, v100
	v_med3_f32 v101, v103, s61, v172
	v_mul_f32_e32 v103, 0x3fd9db23, v96
	v_rcp_f32_e32 v106, v106
	v_mul_f32_e32 v103, 0xbfb8aa3b, v103
	v_exp_f32_e32 v103, v103
	v_pk_fma_f32 v[98:99], v[98:99], s[20:21], v[246:247] op_sel_hi:[1,0,1]
	v_mul_f32_e32 v102, v102, v106
	v_add_f32_e32 v101, 1.0, v101
	v_min_f32_e32 v98, 0x40e00000, v98
	v_mul_f32_e32 v101, v101, v102
	v_add_f32_e32 v102, 1.0, v103
	v_mul_f32_e32 v103, 0x3fd9db23, v98
	v_rcp_f32_e32 v102, v102
	v_mul_f32_e32 v103, 0xbfb8aa3b, v103
	v_exp_f32_e32 v103, v103
	v_med3_f32 v97, v97, s61, v172
	v_mul_f32_e32 v96, v96, v102
	v_add_f32_e32 v97, 1.0, v97
	v_mul_f32_e32 v96, v97, v96
	v_add_f32_e32 v97, 1.0, v103
	v_rcp_f32_e32 v97, v97
	v_cvt_pk_fp8_f32 v203, v100, v101
	v_med3_f32 v99, v99, s61, v172
	v_mul_f32_e32 v97, v98, v97
	v_add_f32_e32 v98, 1.0, v99
	v_mul_f32_e32 v97, v98, v97
	v_cvt_pk_fp8_f32 v203, v96, v97 op_sel:[0,0,1]
	v_lshlrev_b64 v[112:113], 11, v[144:145]
	v_lshl_add_u64 v[112:113], s[16:17], 0, v[112:113]
	v_lshl_add_u64 v[104:105], v[112:113], 0, v[150:151]
	global_store_dwordx2 v[104:105], v[202:203], off
.LBB0_1164:
	s_or_b64 exec, exec, s[10:11]
	v_add_u32_e32 v96, s39, v163
	v_cmp_gt_i32_e32 vcc, s38, v163
	s_nop 1
	v_cndmask_b32_e32 v144, -1, v96, vcc
	v_cmp_lt_i32_e32 vcc, -1, v144
	s_and_saveexec_b64 s[10:11], vcc
	s_cbranch_execz .LBB0_1166
	v_pk_fma_f32 v[92:93], v[92:93], s[20:21], v[232:233] op_sel_hi:[1,0,1]
	v_pk_fma_f32 v[94:95], v[94:95], s[20:21], v[234:235] op_sel_hi:[1,0,1]
	v_min_f32_e32 v92, 0x40e00000, v92
	v_mul_f32_e32 v98, 0x3fd9db23, v92
	v_mul_f32_e32 v98, 0xbfb8aa3b, v98
	v_exp_f32_e32 v98, v98
	v_min_f32_e32 v94, 0x40e00000, v94
	v_mul_f32_e32 v99, 0x3fd9db23, v94
	v_mul_f32_e32 v99, 0xbfb8aa3b, v99
	v_add_f32_e32 v98, 1.0, v98
	v_rcp_f32_e32 v98, v98
	v_exp_f32_e32 v99, v99
	v_pk_fma_f32 v[88:89], v[88:89], s[20:21], v[236:237] op_sel_hi:[1,0,1]
	v_med3_f32 v93, v93, s61, v172
	v_mul_f32_e32 v92, v92, v98
	v_add_f32_e32 v93, 1.0, v93
	v_min_f32_e32 v88, 0x40e00000, v88
	v_add_f32_e32 v98, 1.0, v99
	v_mul_f32_e32 v92, v93, v92
	v_med3_f32 v93, v95, s61, v172
	v_mul_f32_e32 v95, 0x3fd9db23, v88
	v_rcp_f32_e32 v98, v98
	v_mul_f32_e32 v95, 0xbfb8aa3b, v95
	v_exp_f32_e32 v95, v95
	v_pk_fma_f32 v[90:91], v[90:91], s[20:21], v[238:239] op_sel_hi:[1,0,1]
	v_mul_f32_e32 v94, v94, v98
	v_add_f32_e32 v93, 1.0, v93
	v_min_f32_e32 v90, 0x40e00000, v90
	v_mul_f32_e32 v93, v93, v94
	v_add_f32_e32 v94, 1.0, v95
	v_mul_f32_e32 v95, 0x3fd9db23, v90
	v_rcp_f32_e32 v94, v94
	v_mul_f32_e32 v95, 0xbfb8aa3b, v95
	v_exp_f32_e32 v95, v95
	v_med3_f32 v89, v89, s61, v172
	v_mul_f32_e32 v88, v88, v94
	v_add_f32_e32 v89, 1.0, v89
	v_mul_f32_e32 v88, v89, v88
	v_add_f32_e32 v89, 1.0, v95
	v_rcp_f32_e32 v89, v89
	v_cvt_pk_fp8_f32 v204, v92, v93
	v_med3_f32 v91, v91, s61, v172
	v_mul_f32_e32 v89, v90, v89
	v_add_f32_e32 v90, 1.0, v91
	v_pk_fma_f32 v[84:85], v[84:85], s[20:21], v[240:241] op_sel_hi:[1,0,1]
	v_mul_f32_e32 v89, v90, v89
	v_min_f32_e32 v84, 0x40e00000, v84
	v_cvt_pk_fp8_f32 v204, v88, v89 op_sel:[0,0,1]
	v_mul_f32_e32 v88, 0x3fd9db23, v84
	v_mul_f32_e32 v88, 0xbfb8aa3b, v88
	v_exp_f32_e32 v90, v88
	v_pk_fma_f32 v[86:87], v[86:87], s[20:21], v[242:243] op_sel_hi:[1,0,1]
	v_pk_fma_f32 v[80:81], v[80:81], s[20:21], v[244:245] op_sel_hi:[1,0,1]
	v_min_f32_e32 v86, 0x40e00000, v86
	v_add_f32_e32 v90, 1.0, v90
	v_mul_f32_e32 v91, 0x3fd9db23, v86
	v_rcp_f32_e32 v90, v90
	v_mul_f32_e32 v91, 0xbfb8aa3b, v91
	v_exp_f32_e32 v91, v91
	v_med3_f32 v85, v85, s61, v172
	v_mul_f32_e32 v84, v84, v90
	v_add_f32_e32 v85, 1.0, v85
	v_min_f32_e32 v80, 0x40e00000, v80
	v_add_f32_e32 v90, 1.0, v91
	v_mul_f32_e32 v84, v85, v84
	v_med3_f32 v85, v87, s61, v172
	v_mul_f32_e32 v87, 0x3fd9db23, v80
	v_rcp_f32_e32 v90, v90
	v_mul_f32_e32 v87, 0xbfb8aa3b, v87
	v_exp_f32_e32 v87, v87
	v_pk_fma_f32 v[82:83], v[82:83], s[20:21], v[246:247] op_sel_hi:[1,0,1]
	v_mul_f32_e32 v86, v86, v90
	v_add_f32_e32 v85, 1.0, v85
	v_min_f32_e32 v82, 0x40e00000, v82
	v_mul_f32_e32 v85, v85, v86
	v_add_f32_e32 v86, 1.0, v87
	v_mul_f32_e32 v87, 0x3fd9db23, v82
	v_rcp_f32_e32 v86, v86
	v_mul_f32_e32 v87, 0xbfb8aa3b, v87
	v_exp_f32_e32 v87, v87
	v_med3_f32 v81, v81, s61, v172
	v_mul_f32_e32 v80, v80, v86
	v_add_f32_e32 v81, 1.0, v81
	v_mul_f32_e32 v80, v81, v80
	v_add_f32_e32 v81, 1.0, v87
	v_rcp_f32_e32 v81, v81
	v_cvt_pk_fp8_f32 v205, v84, v85
	v_med3_f32 v83, v83, s61, v172
	v_mul_f32_e32 v81, v82, v81
	v_add_f32_e32 v82, 1.0, v83
	v_mul_f32_e32 v81, v82, v81
	v_cvt_pk_fp8_f32 v205, v80, v81 op_sel:[0,0,1]
	v_lshlrev_b64 v[96:97], 11, v[144:145]
	v_lshl_add_u64 v[96:97], s[16:17], 0, v[96:97]
	v_lshl_add_u64 v[88:89], v[96:97], 0, v[150:151]
	global_store_dwordx2 v[88:89], v[204:205], off
.LBB0_1166:
	s_or_b64 exec, exec, s[10:11]
	v_add_u32_e32 v80, s39, v164
	v_cmp_gt_i32_e32 vcc, s38, v164
	s_nop 1
	v_cndmask_b32_e32 v144, -1, v80, vcc
	v_cmp_lt_i32_e32 vcc, -1, v144
	s_and_saveexec_b64 s[10:11], vcc
	s_cbranch_execz .LBB0_1168
	v_pk_fma_f32 v[76:77], v[76:77], s[20:21], v[232:233] op_sel_hi:[1,0,1]
	v_pk_fma_f32 v[78:79], v[78:79], s[20:21], v[234:235] op_sel_hi:[1,0,1]
	v_min_f32_e32 v76, 0x40e00000, v76
	v_mul_f32_e32 v82, 0x3fd9db23, v76
	v_mul_f32_e32 v82, 0xbfb8aa3b, v82
	v_exp_f32_e32 v82, v82
	v_min_f32_e32 v78, 0x40e00000, v78
	v_mul_f32_e32 v83, 0x3fd9db23, v78
	v_mul_f32_e32 v83, 0xbfb8aa3b, v83
	v_add_f32_e32 v82, 1.0, v82
	v_rcp_f32_e32 v82, v82
	v_exp_f32_e32 v83, v83
	v_pk_fma_f32 v[72:73], v[72:73], s[20:21], v[236:237] op_sel_hi:[1,0,1]
	v_med3_f32 v77, v77, s61, v172
	v_mul_f32_e32 v76, v76, v82
	v_add_f32_e32 v77, 1.0, v77
	v_min_f32_e32 v72, 0x40e00000, v72
	v_add_f32_e32 v82, 1.0, v83
	v_mul_f32_e32 v76, v77, v76
	v_med3_f32 v77, v79, s61, v172
	v_mul_f32_e32 v79, 0x3fd9db23, v72
	v_rcp_f32_e32 v82, v82
	v_mul_f32_e32 v79, 0xbfb8aa3b, v79
	v_exp_f32_e32 v79, v79
	v_pk_fma_f32 v[74:75], v[74:75], s[20:21], v[238:239] op_sel_hi:[1,0,1]
	v_mul_f32_e32 v78, v78, v82
	v_add_f32_e32 v77, 1.0, v77
	v_min_f32_e32 v74, 0x40e00000, v74
	v_mul_f32_e32 v77, v77, v78
	v_add_f32_e32 v78, 1.0, v79
	v_mul_f32_e32 v79, 0x3fd9db23, v74
	v_rcp_f32_e32 v78, v78
	v_mul_f32_e32 v79, 0xbfb8aa3b, v79
	v_exp_f32_e32 v79, v79
	v_med3_f32 v73, v73, s61, v172
	v_mul_f32_e32 v72, v72, v78
	v_add_f32_e32 v73, 1.0, v73
	v_mul_f32_e32 v72, v73, v72
	v_add_f32_e32 v73, 1.0, v79
	v_rcp_f32_e32 v73, v73
	v_cvt_pk_fp8_f32 v206, v76, v77
	v_med3_f32 v75, v75, s61, v172
	v_mul_f32_e32 v73, v74, v73
	v_add_f32_e32 v74, 1.0, v75
	v_pk_fma_f32 v[68:69], v[68:69], s[20:21], v[240:241] op_sel_hi:[1,0,1]
	v_mul_f32_e32 v73, v74, v73
	v_min_f32_e32 v68, 0x40e00000, v68
	v_cvt_pk_fp8_f32 v206, v72, v73 op_sel:[0,0,1]
	v_mul_f32_e32 v72, 0x3fd9db23, v68
	v_mul_f32_e32 v72, 0xbfb8aa3b, v72
	v_exp_f32_e32 v74, v72
	v_pk_fma_f32 v[70:71], v[70:71], s[20:21], v[242:243] op_sel_hi:[1,0,1]
	v_pk_fma_f32 v[64:65], v[64:65], s[20:21], v[244:245] op_sel_hi:[1,0,1]
	v_min_f32_e32 v70, 0x40e00000, v70
	v_add_f32_e32 v74, 1.0, v74
	v_mul_f32_e32 v75, 0x3fd9db23, v70
	v_rcp_f32_e32 v74, v74
	v_mul_f32_e32 v75, 0xbfb8aa3b, v75
	v_exp_f32_e32 v75, v75
	v_med3_f32 v69, v69, s61, v172
	v_mul_f32_e32 v68, v68, v74
	v_add_f32_e32 v69, 1.0, v69
	v_min_f32_e32 v64, 0x40e00000, v64
	v_add_f32_e32 v74, 1.0, v75
	v_mul_f32_e32 v68, v69, v68
	v_med3_f32 v69, v71, s61, v172
	v_mul_f32_e32 v71, 0x3fd9db23, v64
	v_rcp_f32_e32 v74, v74
	v_mul_f32_e32 v71, 0xbfb8aa3b, v71
	v_exp_f32_e32 v71, v71
	v_pk_fma_f32 v[66:67], v[66:67], s[20:21], v[246:247] op_sel_hi:[1,0,1]
	v_mul_f32_e32 v70, v70, v74
	v_add_f32_e32 v69, 1.0, v69
	v_min_f32_e32 v66, 0x40e00000, v66
	v_mul_f32_e32 v69, v69, v70
	v_add_f32_e32 v70, 1.0, v71
	v_mul_f32_e32 v71, 0x3fd9db23, v66
	v_rcp_f32_e32 v70, v70
	v_mul_f32_e32 v71, 0xbfb8aa3b, v71
	v_exp_f32_e32 v71, v71
	v_med3_f32 v65, v65, s61, v172
	v_mul_f32_e32 v64, v64, v70
	v_add_f32_e32 v65, 1.0, v65
	v_mul_f32_e32 v64, v65, v64
	v_add_f32_e32 v65, 1.0, v71
	v_rcp_f32_e32 v65, v65
	v_cvt_pk_fp8_f32 v207, v68, v69
	v_med3_f32 v67, v67, s61, v172
	v_mul_f32_e32 v65, v66, v65
	v_add_f32_e32 v66, 1.0, v67
	v_mul_f32_e32 v65, v66, v65
	v_cvt_pk_fp8_f32 v207, v64, v65 op_sel:[0,0,1]
	v_lshlrev_b64 v[80:81], 11, v[144:145]
	v_lshl_add_u64 v[80:81], s[16:17], 0, v[80:81]
	v_lshl_add_u64 v[72:73], v[80:81], 0, v[150:151]
	global_store_dwordx2 v[72:73], v[206:207], off
.LBB0_1168:
	s_or_b64 exec, exec, s[10:11]
	v_add_u32_e32 v64, s39, v165
	v_cmp_gt_i32_e32 vcc, s38, v165
	s_nop 1
	v_cndmask_b32_e32 v144, -1, v64, vcc
	v_cmp_lt_i32_e32 vcc, -1, v144
	s_and_saveexec_b64 s[10:11], vcc
	s_cbranch_execz .LBB0_1170
	v_pk_fma_f32 v[60:61], v[60:61], s[20:21], v[232:233] op_sel_hi:[1,0,1]
	v_pk_fma_f32 v[62:63], v[62:63], s[20:21], v[234:235] op_sel_hi:[1,0,1]
	v_min_f32_e32 v60, 0x40e00000, v60
	v_mul_f32_e32 v66, 0x3fd9db23, v60
	v_mul_f32_e32 v66, 0xbfb8aa3b, v66
	v_exp_f32_e32 v66, v66
	v_min_f32_e32 v62, 0x40e00000, v62
	v_mul_f32_e32 v67, 0x3fd9db23, v62
	v_mul_f32_e32 v67, 0xbfb8aa3b, v67
	v_add_f32_e32 v66, 1.0, v66
	v_rcp_f32_e32 v66, v66
	v_exp_f32_e32 v67, v67
	v_pk_fma_f32 v[56:57], v[56:57], s[20:21], v[236:237] op_sel_hi:[1,0,1]
	v_med3_f32 v61, v61, s61, v172
	v_mul_f32_e32 v60, v60, v66
	v_add_f32_e32 v61, 1.0, v61
	v_min_f32_e32 v56, 0x40e00000, v56
	v_add_f32_e32 v66, 1.0, v67
	v_mul_f32_e32 v60, v61, v60
	v_med3_f32 v61, v63, s61, v172
	v_mul_f32_e32 v63, 0x3fd9db23, v56
	v_rcp_f32_e32 v66, v66
	v_mul_f32_e32 v63, 0xbfb8aa3b, v63
	v_exp_f32_e32 v63, v63
	v_pk_fma_f32 v[58:59], v[58:59], s[20:21], v[238:239] op_sel_hi:[1,0,1]
	v_mul_f32_e32 v62, v62, v66
	v_add_f32_e32 v61, 1.0, v61
	v_min_f32_e32 v58, 0x40e00000, v58
	v_mul_f32_e32 v61, v61, v62
	v_add_f32_e32 v62, 1.0, v63
	v_mul_f32_e32 v63, 0x3fd9db23, v58
	v_rcp_f32_e32 v62, v62
	v_mul_f32_e32 v63, 0xbfb8aa3b, v63
	v_exp_f32_e32 v63, v63
	v_med3_f32 v57, v57, s61, v172
	v_mul_f32_e32 v56, v56, v62
	v_add_f32_e32 v57, 1.0, v57
	v_mul_f32_e32 v56, v57, v56
	v_add_f32_e32 v57, 1.0, v63
	v_rcp_f32_e32 v57, v57
	v_cvt_pk_fp8_f32 v208, v60, v61
	v_med3_f32 v59, v59, s61, v172
	v_mul_f32_e32 v57, v58, v57
	v_add_f32_e32 v58, 1.0, v59
	v_pk_fma_f32 v[52:53], v[52:53], s[20:21], v[240:241] op_sel_hi:[1,0,1]
	v_mul_f32_e32 v57, v58, v57
	v_min_f32_e32 v52, 0x40e00000, v52
	v_cvt_pk_fp8_f32 v208, v56, v57 op_sel:[0,0,1]
	v_mul_f32_e32 v56, 0x3fd9db23, v52
	v_mul_f32_e32 v56, 0xbfb8aa3b, v56
	v_exp_f32_e32 v58, v56
	v_pk_fma_f32 v[54:55], v[54:55], s[20:21], v[242:243] op_sel_hi:[1,0,1]
	v_pk_fma_f32 v[48:49], v[48:49], s[20:21], v[244:245] op_sel_hi:[1,0,1]
	v_min_f32_e32 v54, 0x40e00000, v54
	v_add_f32_e32 v58, 1.0, v58
	v_mul_f32_e32 v59, 0x3fd9db23, v54
	v_rcp_f32_e32 v58, v58
	v_mul_f32_e32 v59, 0xbfb8aa3b, v59
	v_exp_f32_e32 v59, v59
	v_med3_f32 v53, v53, s61, v172
	v_mul_f32_e32 v52, v52, v58
	v_add_f32_e32 v53, 1.0, v53
	v_min_f32_e32 v48, 0x40e00000, v48
	v_add_f32_e32 v58, 1.0, v59
	v_mul_f32_e32 v52, v53, v52
	v_med3_f32 v53, v55, s61, v172
	v_mul_f32_e32 v55, 0x3fd9db23, v48
	v_rcp_f32_e32 v58, v58
	v_mul_f32_e32 v55, 0xbfb8aa3b, v55
	v_exp_f32_e32 v55, v55
	v_pk_fma_f32 v[50:51], v[50:51], s[20:21], v[246:247] op_sel_hi:[1,0,1]
	v_mul_f32_e32 v54, v54, v58
	v_add_f32_e32 v53, 1.0, v53
	v_min_f32_e32 v50, 0x40e00000, v50
	v_mul_f32_e32 v53, v53, v54
	v_add_f32_e32 v54, 1.0, v55
	v_mul_f32_e32 v55, 0x3fd9db23, v50
	v_rcp_f32_e32 v54, v54
	v_mul_f32_e32 v55, 0xbfb8aa3b, v55
	v_exp_f32_e32 v55, v55
	v_med3_f32 v49, v49, s61, v172
	v_mul_f32_e32 v48, v48, v54
	v_add_f32_e32 v49, 1.0, v49
	v_mul_f32_e32 v48, v49, v48
	v_add_f32_e32 v49, 1.0, v55
	v_rcp_f32_e32 v49, v49
	v_cvt_pk_fp8_f32 v209, v52, v53
	v_med3_f32 v51, v51, s61, v172
	v_mul_f32_e32 v49, v50, v49
	v_add_f32_e32 v50, 1.0, v51
	v_mul_f32_e32 v49, v50, v49
	v_cvt_pk_fp8_f32 v209, v48, v49 op_sel:[0,0,1]
	v_lshlrev_b64 v[64:65], 11, v[144:145]
	v_lshl_add_u64 v[64:65], s[16:17], 0, v[64:65]
	v_lshl_add_u64 v[56:57], v[64:65], 0, v[150:151]
	global_store_dwordx2 v[56:57], v[208:209], off
.LBB0_1170:
	s_or_b64 exec, exec, s[10:11]
	v_add_u32_e32 v48, s39, v166
	v_cmp_gt_i32_e32 vcc, s38, v166
	s_nop 1
	v_cndmask_b32_e32 v144, -1, v48, vcc
	v_cmp_lt_i32_e32 vcc, -1, v144
	s_and_saveexec_b64 s[10:11], vcc
	s_cbranch_execz .LBB0_1172
	v_pk_fma_f32 v[44:45], v[44:45], s[20:21], v[232:233] op_sel_hi:[1,0,1]
	v_pk_fma_f32 v[46:47], v[46:47], s[20:21], v[234:235] op_sel_hi:[1,0,1]
	v_min_f32_e32 v44, 0x40e00000, v44
	v_mul_f32_e32 v50, 0x3fd9db23, v44
	v_mul_f32_e32 v50, 0xbfb8aa3b, v50
	v_exp_f32_e32 v50, v50
	v_min_f32_e32 v46, 0x40e00000, v46
	v_mul_f32_e32 v51, 0x3fd9db23, v46
	v_mul_f32_e32 v51, 0xbfb8aa3b, v51
	v_add_f32_e32 v50, 1.0, v50
	v_rcp_f32_e32 v50, v50
	v_exp_f32_e32 v51, v51
	v_pk_fma_f32 v[40:41], v[40:41], s[20:21], v[236:237] op_sel_hi:[1,0,1]
	v_med3_f32 v45, v45, s61, v172
	v_mul_f32_e32 v44, v44, v50
	v_add_f32_e32 v45, 1.0, v45
	v_min_f32_e32 v40, 0x40e00000, v40
	v_add_f32_e32 v50, 1.0, v51
	v_mul_f32_e32 v44, v45, v44
	v_med3_f32 v45, v47, s61, v172
	v_mul_f32_e32 v47, 0x3fd9db23, v40
	v_rcp_f32_e32 v50, v50
	v_mul_f32_e32 v47, 0xbfb8aa3b, v47
	v_exp_f32_e32 v47, v47
	v_pk_fma_f32 v[42:43], v[42:43], s[20:21], v[238:239] op_sel_hi:[1,0,1]
	v_mul_f32_e32 v46, v46, v50
	v_add_f32_e32 v45, 1.0, v45
	v_min_f32_e32 v42, 0x40e00000, v42
	v_mul_f32_e32 v45, v45, v46
	v_add_f32_e32 v46, 1.0, v47
	v_mul_f32_e32 v47, 0x3fd9db23, v42
	v_rcp_f32_e32 v46, v46
	v_mul_f32_e32 v47, 0xbfb8aa3b, v47
	v_exp_f32_e32 v47, v47
	v_med3_f32 v41, v41, s61, v172
	v_mul_f32_e32 v40, v40, v46
	v_add_f32_e32 v41, 1.0, v41
	v_mul_f32_e32 v40, v41, v40
	v_add_f32_e32 v41, 1.0, v47
	v_rcp_f32_e32 v41, v41
	v_cvt_pk_fp8_f32 v210, v44, v45
	v_med3_f32 v43, v43, s61, v172
	v_mul_f32_e32 v41, v42, v41
	v_add_f32_e32 v42, 1.0, v43
	v_pk_fma_f32 v[36:37], v[36:37], s[20:21], v[240:241] op_sel_hi:[1,0,1]
	v_mul_f32_e32 v41, v42, v41
	v_min_f32_e32 v36, 0x40e00000, v36
	v_cvt_pk_fp8_f32 v210, v40, v41 op_sel:[0,0,1]
	v_mul_f32_e32 v40, 0x3fd9db23, v36
	v_mul_f32_e32 v40, 0xbfb8aa3b, v40
	v_exp_f32_e32 v42, v40
	v_pk_fma_f32 v[38:39], v[38:39], s[20:21], v[242:243] op_sel_hi:[1,0,1]
	v_pk_fma_f32 v[32:33], v[32:33], s[20:21], v[244:245] op_sel_hi:[1,0,1]
	v_min_f32_e32 v38, 0x40e00000, v38
	v_add_f32_e32 v42, 1.0, v42
	v_mul_f32_e32 v43, 0x3fd9db23, v38
	v_rcp_f32_e32 v42, v42
	v_mul_f32_e32 v43, 0xbfb8aa3b, v43
	v_exp_f32_e32 v43, v43
	v_med3_f32 v37, v37, s61, v172
	v_mul_f32_e32 v36, v36, v42
	v_add_f32_e32 v37, 1.0, v37
	v_min_f32_e32 v32, 0x40e00000, v32
	v_add_f32_e32 v42, 1.0, v43
	v_mul_f32_e32 v36, v37, v36
	v_med3_f32 v37, v39, s61, v172
	v_mul_f32_e32 v39, 0x3fd9db23, v32
	v_rcp_f32_e32 v42, v42
	v_mul_f32_e32 v39, 0xbfb8aa3b, v39
	v_exp_f32_e32 v39, v39
	v_pk_fma_f32 v[34:35], v[34:35], s[20:21], v[246:247] op_sel_hi:[1,0,1]
	v_mul_f32_e32 v38, v38, v42
	v_add_f32_e32 v37, 1.0, v37
	v_min_f32_e32 v34, 0x40e00000, v34
	v_mul_f32_e32 v37, v37, v38
	v_add_f32_e32 v38, 1.0, v39
	v_mul_f32_e32 v39, 0x3fd9db23, v34
	v_rcp_f32_e32 v38, v38
	v_mul_f32_e32 v39, 0xbfb8aa3b, v39
	v_exp_f32_e32 v39, v39
	v_med3_f32 v33, v33, s61, v172
	v_mul_f32_e32 v32, v32, v38
	v_add_f32_e32 v33, 1.0, v33
	v_mul_f32_e32 v32, v33, v32
	v_add_f32_e32 v33, 1.0, v39
	v_rcp_f32_e32 v33, v33
	v_cvt_pk_fp8_f32 v211, v36, v37
	v_med3_f32 v35, v35, s61, v172
	v_mul_f32_e32 v33, v34, v33
	v_add_f32_e32 v34, 1.0, v35
	v_mul_f32_e32 v33, v34, v33
	v_cvt_pk_fp8_f32 v211, v32, v33 op_sel:[0,0,1]
	v_lshlrev_b64 v[48:49], 11, v[144:145]
	v_lshl_add_u64 v[48:49], s[16:17], 0, v[48:49]
	v_lshl_add_u64 v[40:41], v[48:49], 0, v[150:151]
	global_store_dwordx2 v[40:41], v[210:211], off
.LBB0_1172:
	s_or_b64 exec, exec, s[10:11]
	v_add_u32_e32 v32, s39, v167
	v_cmp_gt_i32_e32 vcc, s38, v167
	s_nop 1
	v_cndmask_b32_e32 v144, -1, v32, vcc
	v_cmp_lt_i32_e32 vcc, -1, v144
	s_and_saveexec_b64 s[10:11], vcc
	s_cbranch_execz .LBB0_1174
	v_pk_fma_f32 v[28:29], v[28:29], s[20:21], v[232:233] op_sel_hi:[1,0,1]
	v_pk_fma_f32 v[30:31], v[30:31], s[20:21], v[234:235] op_sel_hi:[1,0,1]
	v_min_f32_e32 v28, 0x40e00000, v28
	v_mul_f32_e32 v34, 0x3fd9db23, v28
	v_mul_f32_e32 v34, 0xbfb8aa3b, v34
	v_exp_f32_e32 v34, v34
	v_min_f32_e32 v30, 0x40e00000, v30
	v_mul_f32_e32 v35, 0x3fd9db23, v30
	v_mul_f32_e32 v35, 0xbfb8aa3b, v35
	v_add_f32_e32 v34, 1.0, v34
	v_rcp_f32_e32 v34, v34
	v_exp_f32_e32 v35, v35
	v_pk_fma_f32 v[24:25], v[24:25], s[20:21], v[236:237] op_sel_hi:[1,0,1]
	v_med3_f32 v29, v29, s61, v172
	v_mul_f32_e32 v28, v28, v34
	v_add_f32_e32 v29, 1.0, v29
	v_min_f32_e32 v24, 0x40e00000, v24
	v_add_f32_e32 v34, 1.0, v35
	v_mul_f32_e32 v28, v29, v28
	v_med3_f32 v29, v31, s61, v172
	v_mul_f32_e32 v31, 0x3fd9db23, v24
	v_rcp_f32_e32 v34, v34
	v_mul_f32_e32 v31, 0xbfb8aa3b, v31
	v_exp_f32_e32 v31, v31
	v_pk_fma_f32 v[26:27], v[26:27], s[20:21], v[238:239] op_sel_hi:[1,0,1]
	v_mul_f32_e32 v30, v30, v34
	v_add_f32_e32 v29, 1.0, v29
	v_min_f32_e32 v26, 0x40e00000, v26
	v_mul_f32_e32 v29, v29, v30
	v_add_f32_e32 v30, 1.0, v31
	v_mul_f32_e32 v31, 0x3fd9db23, v26
	v_rcp_f32_e32 v30, v30
	v_mul_f32_e32 v31, 0xbfb8aa3b, v31
	v_exp_f32_e32 v31, v31
	v_med3_f32 v25, v25, s61, v172
	v_mul_f32_e32 v24, v24, v30
	v_add_f32_e32 v25, 1.0, v25
	v_mul_f32_e32 v24, v25, v24
	v_add_f32_e32 v25, 1.0, v31
	v_rcp_f32_e32 v25, v25
	v_cvt_pk_fp8_f32 v212, v28, v29
	v_med3_f32 v27, v27, s61, v172
	v_mul_f32_e32 v25, v26, v25
	v_add_f32_e32 v26, 1.0, v27
	v_pk_fma_f32 v[20:21], v[20:21], s[20:21], v[240:241] op_sel_hi:[1,0,1]
	v_mul_f32_e32 v25, v26, v25
	v_min_f32_e32 v20, 0x40e00000, v20
	v_cvt_pk_fp8_f32 v212, v24, v25 op_sel:[0,0,1]
	v_mul_f32_e32 v24, 0x3fd9db23, v20
	v_mul_f32_e32 v24, 0xbfb8aa3b, v24
	v_exp_f32_e32 v26, v24
	v_pk_fma_f32 v[22:23], v[22:23], s[20:21], v[242:243] op_sel_hi:[1,0,1]
	v_pk_fma_f32 v[16:17], v[16:17], s[20:21], v[244:245] op_sel_hi:[1,0,1]
	v_min_f32_e32 v22, 0x40e00000, v22
	v_add_f32_e32 v26, 1.0, v26
	v_mul_f32_e32 v27, 0x3fd9db23, v22
	v_rcp_f32_e32 v26, v26
	v_mul_f32_e32 v27, 0xbfb8aa3b, v27
	v_exp_f32_e32 v27, v27
	v_med3_f32 v21, v21, s61, v172
	v_mul_f32_e32 v20, v20, v26
	v_add_f32_e32 v21, 1.0, v21
	v_min_f32_e32 v16, 0x40e00000, v16
	v_add_f32_e32 v26, 1.0, v27
	v_mul_f32_e32 v20, v21, v20
	v_med3_f32 v21, v23, s61, v172
	v_mul_f32_e32 v23, 0x3fd9db23, v16
	v_rcp_f32_e32 v26, v26
	v_mul_f32_e32 v23, 0xbfb8aa3b, v23
	v_exp_f32_e32 v23, v23
	v_pk_fma_f32 v[18:19], v[18:19], s[20:21], v[246:247] op_sel_hi:[1,0,1]
	v_mul_f32_e32 v22, v22, v26
	v_add_f32_e32 v21, 1.0, v21
	v_min_f32_e32 v18, 0x40e00000, v18
	v_mul_f32_e32 v21, v21, v22
	v_add_f32_e32 v22, 1.0, v23
	v_mul_f32_e32 v23, 0x3fd9db23, v18
	v_rcp_f32_e32 v22, v22
	v_mul_f32_e32 v23, 0xbfb8aa3b, v23
	v_exp_f32_e32 v23, v23
	v_med3_f32 v17, v17, s61, v172
	v_mul_f32_e32 v16, v16, v22
	v_add_f32_e32 v17, 1.0, v17
	v_mul_f32_e32 v16, v17, v16
	v_add_f32_e32 v17, 1.0, v23
	v_rcp_f32_e32 v17, v17
	v_cvt_pk_fp8_f32 v213, v20, v21
	v_med3_f32 v19, v19, s61, v172
	v_mul_f32_e32 v17, v18, v17
	v_add_f32_e32 v18, 1.0, v19
	v_mul_f32_e32 v17, v18, v17
	v_cvt_pk_fp8_f32 v213, v16, v17 op_sel:[0,0,1]
	v_lshlrev_b64 v[32:33], 11, v[144:145]
	v_lshl_add_u64 v[32:33], s[16:17], 0, v[32:33]
	v_lshl_add_u64 v[24:25], v[32:33], 0, v[150:151]
	global_store_dwordx2 v[24:25], v[212:213], off
.LBB0_1174:
	s_or_b64 exec, exec, s[10:11]
	v_add_u32_e32 v16, s39, v168
	v_cmp_gt_i32_e32 vcc, s38, v168
	s_nop 1
	v_cndmask_b32_e32 v144, -1, v16, vcc
	v_cmp_lt_i32_e32 vcc, -1, v144
	s_and_saveexec_b64 s[10:11], vcc
	s_cbranch_execz .LBB0_1176
	v_pk_fma_f32 v[12:13], v[12:13], s[20:21], v[232:233] op_sel_hi:[1,0,1]
	v_pk_fma_f32 v[14:15], v[14:15], s[20:21], v[234:235] op_sel_hi:[1,0,1]
	v_min_f32_e32 v12, 0x40e00000, v12
	v_mul_f32_e32 v18, 0x3fd9db23, v12
	v_mul_f32_e32 v18, 0xbfb8aa3b, v18
	v_exp_f32_e32 v18, v18
	v_min_f32_e32 v14, 0x40e00000, v14
	v_mul_f32_e32 v19, 0x3fd9db23, v14
	v_mul_f32_e32 v19, 0xbfb8aa3b, v19
	v_add_f32_e32 v18, 1.0, v18
	v_rcp_f32_e32 v18, v18
	v_exp_f32_e32 v19, v19
	v_pk_fma_f32 v[8:9], v[8:9], s[20:21], v[236:237] op_sel_hi:[1,0,1]
	v_med3_f32 v13, v13, s61, v172
	v_mul_f32_e32 v12, v12, v18
	v_add_f32_e32 v13, 1.0, v13
	v_min_f32_e32 v8, 0x40e00000, v8
	v_add_f32_e32 v18, 1.0, v19
	v_mul_f32_e32 v12, v13, v12
	v_med3_f32 v13, v15, s61, v172
	v_mul_f32_e32 v15, 0x3fd9db23, v8
	v_rcp_f32_e32 v18, v18
	v_mul_f32_e32 v15, 0xbfb8aa3b, v15
	v_exp_f32_e32 v15, v15
	v_pk_fma_f32 v[10:11], v[10:11], s[20:21], v[238:239] op_sel_hi:[1,0,1]
	v_mul_f32_e32 v14, v14, v18
	v_add_f32_e32 v13, 1.0, v13
	v_min_f32_e32 v10, 0x40e00000, v10
	v_mul_f32_e32 v13, v13, v14
	v_add_f32_e32 v14, 1.0, v15
	v_mul_f32_e32 v15, 0x3fd9db23, v10
	v_rcp_f32_e32 v14, v14
	v_mul_f32_e32 v15, 0xbfb8aa3b, v15
	v_exp_f32_e32 v15, v15
	v_med3_f32 v9, v9, s61, v172
	v_mul_f32_e32 v8, v8, v14
	v_add_f32_e32 v9, 1.0, v9
	v_mul_f32_e32 v8, v9, v8
	v_add_f32_e32 v9, 1.0, v15
	v_rcp_f32_e32 v9, v9
	v_cvt_pk_fp8_f32 v214, v12, v13
	v_med3_f32 v11, v11, s61, v172
	v_mul_f32_e32 v9, v10, v9
	v_add_f32_e32 v10, 1.0, v11
	v_pk_fma_f32 v[4:5], v[4:5], s[20:21], v[240:241] op_sel_hi:[1,0,1]
	v_mul_f32_e32 v9, v10, v9
	v_min_f32_e32 v4, 0x40e00000, v4
	v_cvt_pk_fp8_f32 v214, v8, v9 op_sel:[0,0,1]
	v_mul_f32_e32 v8, 0x3fd9db23, v4
	v_mul_f32_e32 v8, 0xbfb8aa3b, v8
	v_exp_f32_e32 v10, v8
	v_pk_fma_f32 v[6:7], v[6:7], s[20:21], v[242:243] op_sel_hi:[1,0,1]
	v_pk_fma_f32 v[0:1], v[0:1], s[20:21], v[244:245] op_sel_hi:[1,0,1]
	v_min_f32_e32 v6, 0x40e00000, v6
	v_add_f32_e32 v10, 1.0, v10
	v_mul_f32_e32 v11, 0x3fd9db23, v6
	v_rcp_f32_e32 v10, v10
	v_mul_f32_e32 v11, 0xbfb8aa3b, v11
	v_exp_f32_e32 v11, v11
	v_med3_f32 v5, v5, s61, v172
	v_mul_f32_e32 v4, v4, v10
	v_add_f32_e32 v5, 1.0, v5
	v_min_f32_e32 v0, 0x40e00000, v0
	v_add_f32_e32 v10, 1.0, v11
	v_mul_f32_e32 v4, v5, v4
	v_med3_f32 v5, v7, s61, v172
	v_mul_f32_e32 v7, 0x3fd9db23, v0
	v_rcp_f32_e32 v10, v10
	v_mul_f32_e32 v7, 0xbfb8aa3b, v7
	v_exp_f32_e32 v7, v7
	v_pk_fma_f32 v[2:3], v[2:3], s[20:21], v[246:247] op_sel_hi:[1,0,1]
	v_mul_f32_e32 v6, v6, v10
	v_add_f32_e32 v5, 1.0, v5
	v_min_f32_e32 v2, 0x40e00000, v2
	v_mul_f32_e32 v5, v5, v6
	v_add_f32_e32 v6, 1.0, v7
	v_mul_f32_e32 v7, 0x3fd9db23, v2
	v_rcp_f32_e32 v6, v6
	v_mul_f32_e32 v7, 0xbfb8aa3b, v7
	v_exp_f32_e32 v7, v7
	v_med3_f32 v1, v1, s61, v172
	v_mul_f32_e32 v0, v0, v6
	v_add_f32_e32 v1, 1.0, v1
	v_mul_f32_e32 v0, v1, v0
	v_add_f32_e32 v1, 1.0, v7
	v_rcp_f32_e32 v1, v1
	v_cvt_pk_fp8_f32 v215, v4, v5
	v_med3_f32 v3, v3, s61, v172
	v_mul_f32_e32 v1, v2, v1
	v_add_f32_e32 v2, 1.0, v3
	v_mul_f32_e32 v1, v2, v1
	v_cvt_pk_fp8_f32 v215, v0, v1 op_sel:[0,0,1]
	v_lshlrev_b64 v[16:17], 11, v[144:145]
	v_lshl_add_u64 v[16:17], s[16:17], 0, v[16:17]
	v_lshl_add_u64 v[8:9], v[16:17], 0, v[150:151]
	global_store_dwordx2 v[8:9], v[214:215], off

.LBB0_1243:
	s_andn2_b64 vcc, exec, s[2:3]
	s_cbranch_vccnz .LBB0_1277
	s_add_u32 s20, s92, 0x52ee1c00
	s_addc_u32 s2, s93, 0
	s_add_u32 s24, s92, 0x48ee1c00
	s_addc_u32 s3, s93, 0
	s_lshl_b32 s5, s86, 10
	v_lshl_or_b32 v0, v132, 4, s5
	v_ashrrev_i32_e32 v1, 31, v0
	v_lshrrev_b32_e32 v1, 22, v1
	v_add_u32_e32 v1, v0, v1
	v_ashrrev_i32_e32 v1, 10, v1
	v_mul_i32_i24_e32 v2, 0x400, v1
	v_sub_u32_e32 v2, v0, v2
	v_lshrrev_b32_e32 v3, 4, v2
	v_bitop3_b32 v2, v3, v2, 32 bitop3:0x6c
	s_waitcnt vmcnt(8)
	v_ashrrev_i32_e32 v4, 31, v2
	v_lshrrev_b32_e32 v4, 26, v4
	v_lshlrev_b32_e32 v3, 3, v1
	v_add_u32_e32 v4, v2, v4
	v_and_b32_e32 v3, -16, v3
	v_ashrrev_i32_e32 v5, 6, v4
	v_add_u32_e32 v151, v5, v3
	v_and_b32_e32 v3, 0xc0, v4
	v_sub_u32_e32 v2, v2, v3
	v_mov_b32_e32 v3, 1
	v_lshlrev_b32_e32 v1, 5, v1
	v_ashrrev_i16_sdwa v2, v3, sext(v2) dst_sel:DWORD dst_unused:UNUSED_PAD src0_sel:DWORD src1_sel:BYTE_0
	v_and_b32_e32 v1, 32, v1
	v_bfe_i32 v2, v2, 0, 16
	v_add_u32_e32 v0, 0x2000, v0
	v_add_lshl_u32 v153, v1, v2, 1
	v_ashrrev_i32_e32 v1, 31, v0
	v_lshrrev_b32_e32 v1, 22, v1
	v_add_u32_e32 v1, v0, v1
	v_ashrrev_i32_e32 v1, 10, v1
	v_mul_i32_i24_e32 v2, 0x400, v1
	v_lshlrev_b32_e32 v4, 1, v151
	v_lshrrev_b32_e32 v6, 2, v151
	v_and_b32_e32 v5, 3, v5
	s_mov_b32 s6, 0x1fffe0
	v_sub_u32_e32 v0, v0, v2
	v_and_b32_e32 v4, 24, v4
	v_and_b32_e32 v6, 4, v6
	v_and_or_b32 v5, v151, s6, v5
	v_lshrrev_b32_e32 v2, 4, v0
	v_or3_b32 v4, v5, v6, v4
	v_bitop3_b32 v0, v2, v0, 32 bitop3:0x6c
	v_lshl_add_u32 v155, v4, 11, v153
	v_and_b32_e32 v200, 0x3c000, v155
	v_add_u32_e32 v155, v155, v200
	v_ashrrev_i32_e32 v4, 31, v0
	v_lshrrev_b32_e32 v4, 26, v4
	v_lshlrev_b32_e32 v2, 3, v1
	v_add_u32_e32 v4, v0, v4
	v_and_b32_e32 v2, -16, v2
	v_ashrrev_i32_e32 v5, 6, v4
	v_add_u32_e32 v157, v5, v2
	v_and_b32_e32 v2, 0xffc0, v4
	v_sub_u32_e32 v0, v0, v2
	v_lshrrev_b16_e32 v2, 7, v0
	v_and_b32_e32 v2, 1, v2
	s_and_b32 s21, s2, 0xffff
	s_add_i32 s2, s81, -1
	v_add_u32_e32 v166, 0x80, v151
	v_add_u32_e32 v167, 0x80, v157
	v_add_u16_e32 v0, v0, v2
	v_min_i32_e32 v128, s2, v151
	v_min_i32_e32 v129, s2, v157
	v_min_i32_e32 v130, s2, v166
	v_min_i32_e32 v131, s2, v167
	v_lshlrev_b32_e32 v133, 21, v146
	s_lshl_b32 s2, s1, 18
	v_lshlrev_b32_e32 v1, 5, v1
	v_ashrrev_i16_sdwa v0, v3, sext(v0) dst_sel:DWORD dst_unused:UNUSED_PAD src0_sel:DWORD src1_sel:BYTE_0
	v_lshlrev_b32_e32 v2, 1, v157
	v_lshrrev_b32_e32 v3, 2, v157
	v_and_b32_e32 v4, 3, v5
	v_add_u32_e32 v133, s2, v133
	s_add_i32 s42, s5, 0
	v_and_b32_e32 v1, 32, v1
	v_bfe_i32 v0, v0, 0, 16
	v_and_b32_e32 v2, 24, v2
	v_and_b32_e32 v3, 4, v3
	v_and_or_b32 v4, v157, s6, v4
	s_mov_b32 s23, 0x20000
	s_mov_b32 s22, -1
	v_readfirstlane_b32 s2, v133
	s_add_i32 s43, s42, 0x10000
	v_or3_b32 v2, v4, v3, v2
	v_add_lshl_u32 v159, v1, v0, 1
	s_and_b32 s25, s3, 0xffff
	s_mov_b32 s26, s22
	s_mov_b32 s27, s23
	s_lshl_b32 s6, s2, 1
	s_mov_b32 m0, s43
	s_add_i32 s44, s42, 0x12000
	v_lshl_add_u32 v161, v2, 11, v159
	v_and_b32_e32 v200, 0x3c000, v161
	v_add_u32_e32 v161, v161, v200
	v_mov_b64 v[124:125], 0
	v_mov_b64 v[126:127], 0
	v_mov_b64 v[120:121], 0
	v_mov_b64 v[122:123], 0
	v_mov_b64 v[108:109], 0
	v_mov_b64 v[110:111], 0
	v_mov_b64 v[104:105], 0
	v_mov_b64 v[106:107], 0
	v_mov_b64 v[92:93], 0
	v_mov_b64 v[94:95], 0
	v_mov_b64 v[88:89], 0
	v_mov_b64 v[90:91], 0
	v_mov_b64 v[76:77], 0
	v_mov_b64 v[78:79], 0
	v_mov_b64 v[72:73], 0
	v_mov_b64 v[74:75], 0
	v_mov_b64 v[116:117], 0
	v_mov_b64 v[118:119], 0
	v_mov_b64 v[112:113], 0
	v_mov_b64 v[114:115], 0
	v_mov_b64 v[100:101], 0
	v_mov_b64 v[102:103], 0
	v_mov_b64 v[96:97], 0
	v_mov_b64 v[98:99], 0
	v_mov_b64 v[84:85], 0
	v_mov_b64 v[86:87], 0
	v_mov_b64 v[80:81], 0
	v_mov_b64 v[82:83], 0
	v_mov_b64 v[68:69], 0
	v_mov_b64 v[70:71], 0
	v_mov_b64 v[64:65], 0
	v_mov_b64 v[66:67], 0
	s_waitcnt vmcnt(7)
	v_mov_b64 v[60:61], 0
	v_mov_b64 v[62:63], 0
	s_waitcnt vmcnt(4)
	v_mov_b64 v[56:57], 0
	v_mov_b64 v[58:59], 0
	v_mov_b64 v[44:45], 0
	v_mov_b64 v[46:47], 0
	v_mov_b64 v[40:41], 0
	v_mov_b64 v[42:43], 0
	v_mov_b64 v[28:29], 0
	v_mov_b64 v[30:31], 0
	v_mov_b64 v[24:25], 0
	v_mov_b64 v[26:27], 0
	v_mov_b64 v[12:13], 0
	v_mov_b64 v[14:15], 0
	v_mov_b64 v[8:9], 0
	v_mov_b64 v[10:11], 0
	v_mov_b64 v[52:53], 0
	v_mov_b64 v[54:55], 0
	v_mov_b64 v[48:49], 0
	v_mov_b64 v[50:51], 0
	v_mov_b64 v[36:37], 0
	v_mov_b64 v[38:39], 0
	v_mov_b64 v[32:33], 0
	v_mov_b64 v[34:35], 0
	v_mov_b64 v[20:21], 0
	v_mov_b64 v[22:23], 0
	v_mov_b64 v[16:17], 0
	v_mov_b64 v[18:19], 0
	v_mov_b64 v[4:5], 0
	v_mov_b64 v[6:7], 0
	v_mov_b64 v[0:1], 0
	v_mov_b64 v[2:3], 0
	buffer_load_dwordx4 v155, s[24:27], s6 offen lds
	s_mov_b32 m0, s44
	s_add_i32 s45, s42, 0x14000
	buffer_load_dwordx4 v161, s[24:27], s6 offen lds
	s_add_i32 s2, s6, 0x4000
	s_mov_b32 m0, s45
	s_add_i32 s46, s42, 0x16000
	v_add_u32_e32 v128, s4, v128
	buffer_load_dwordx4 v155, s[24:27], s2 offen lds
	s_mov_b32 m0, s46
	v_lshl_add_u32 v128, v128, 11, v153
	v_add_u32_e32 v129, s4, v129
	buffer_load_dwordx4 v161, s[24:27], s2 offen lds
	s_mov_b32 m0, s42
	s_add_i32 s47, s42, 0x2000
	v_lshl_add_u32 v129, v129, 11, v159
	v_add_u32_e32 v130, s4, v130
	buffer_load_dwordx4 v128, s[20:23], 0 offen lds
	s_mov_b32 m0, s47
	s_add_i32 s48, s42, 0x4000
	v_lshl_add_u32 v130, v130, 11, v153
	v_add_u32_e32 v131, s4, v131
	buffer_load_dwordx4 v129, s[20:23], 0 offen lds
	s_mov_b32 m0, s48
	s_add_i32 s49, s42, 0x6000
	v_lshl_add_u32 v131, v131, 11, v159
	buffer_load_dwordx4 v130, s[20:23], 0 offen lds
	s_mov_b32 m0, s49
	s_lshr_b32 s2, s90, 8
	buffer_load_dwordx4 v131, s[20:23], 0 offen lds
	s_cmp_eq_u32 s2, 1
	s_movk_i32 s3, 0x80
	s_cselect_b64 s[28:29], -1, 0
	s_cmp_lg_u32 s2, 1
	s_mov_b32 s50, 0
	s_cbranch_scc1 .LBB0_1246
	s_barrier
.LBB0_1246:
	s_add_u32 s30, s92, 0x17ee1c00
	s_addc_u32 s31, s93, 0
	s_add_u32 s34, s92, 0x176e1c00
	s_addc_u32 s35, s93, 0
	s_add_u32 s36, s92, 0x28ee1c00
	s_addc_u32 s37, s93, 0
	s_add_i32 s51, s42, 0x18000
	s_add_i32 s4, s6, 0x80
	s_mov_b32 s26, s22
	s_mov_b32 s27, s23
	s_mov_b32 m0, s51
	s_add_i32 s52, s42, 0x1a000
	s_waitcnt vmcnt(2)
	s_barrier
	buffer_load_dwordx4 v155, s[24:27], s4 offen lds
	s_mov_b32 m0, s52
	s_add_i32 s53, s42, 0x8000
	buffer_load_dwordx4 v161, s[24:27], s4 offen lds
	s_mov_b32 m0, s53
	s_add_i32 s54, s42, 0xa000
	buffer_load_dwordx4 v128, s[20:23], s3 offen lds
	s_mov_b32 m0, s54
	s_add_i32 s55, s42, 0x1c000
	buffer_load_dwordx4 v129, s[20:23], s3 offen lds
	s_add_i32 s3, s6, 0x4080
	s_mov_b32 m0, s55
	s_add_i32 s56, s42, 0x1e000
	buffer_load_dwordx4 v155, s[24:27], s3 offen lds
	s_mov_b32 m0, s56
	v_and_b32_e32 v133, 15, v132
	buffer_load_dwordx4 v161, s[24:27], s3 offen lds
	v_lshrrev_b32_e32 v134, 1, v132
	v_lshrrev_b32_e32 v135, 6, v132
	v_and_b32_e32 v136, 48, v132
	v_lshlrev_b32_e32 v132, 2, v132
	v_lshlrev_b32_e32 v138, 6, v133
	v_and_b32_e32 v132, 32, v132
	s_lshl_b32 s3, s2, 6
	s_lshl_b32 s2, s2, 13
	v_lshlrev_b32_e32 v137, 10, v135
	v_bitop3_b32 v139, v138, v132, v136 bitop3:0x36
	v_or3_b32 v137, v137, s2, v139
	s_lshl_b32 s2, s86, 5
	s_and_b32 s2, s2, 0x60
	s_lshr_b32 s4, s2, 3
	s_add_i32 s57, s42, 0xc000
	s_add_i32 s58, s42, 0xe000
	v_or_b32_e32 v135, s4, v135
	s_cmpk_lt_u32 s90, 0x100
	v_or_b32_e32 v168, s3, v133
	v_or_b32_e32 v136, v138, v136
	v_lshlrev_b32_e32 v135, 10, v135
	s_waitcnt vmcnt(6)
	s_cselect_b64 s[38:39], -1, 0
	s_addk_i32 s3, 0x80
	v_and_b32_e32 v134, 56, v134
	v_bitop3_b32 v132, v136, v135, v132 bitop3:0xde
	v_or_b32_e32 v173, s3, v133
	v_add_u32_e32 v169, s2, v134
	v_lshlrev_b32_e32 v169, 1, v169
	v_or_b32_e32 v170, 16, v168
	v_or_b32_e32 v171, 32, v168
	v_or_b32_e32 v172, 48, v168
	v_or_b32_e32 v174, 16, v173
	v_or_b32_e32 v175, 32, v173
	v_or_b32_e32 v176, 48, v173
	s_add_i32 s59, 0, 0x20084
	s_add_i32 s60, 0, 0x2008c
	s_add_i32 s61, 0, 0x20094
	s_add_i32 s62, 0, 0x2009c
	s_add_i32 s63, 0, 0x200a4
	s_add_i32 s64, 0, 0x200ac
	s_add_i32 s65, 0, 0x200b4
	s_add_i32 s66, 0, 0x200bc
	s_add_i32 s67, 0, 0x200c4
	s_add_i32 s68, 0, 0x200cc
	s_add_i32 s69, 0, 0x200d4
	s_add_i32 s70, 0, 0x200dc
	s_add_i32 s71, 0, 0x200e4
	s_add_i32 s72, 0, 0x200ec
	s_add_i32 s73, 0, 0x200f4
	s_add_i32 s74, 0, 0x200fc
	v_add_u32_e32 v177, 0, v132
	v_add_u32_e32 v178, 0, v137
	v_mov_b32_e32 v179, 0x7f7f7f7f
	v_mov_b32_e32 v145, 0
	s_mov_b32 s40, 0x3c800000
	s_mov_b32 s75, 0xc3e00000
	v_mov_b32_e32 v180, 0x43e00000
	s_barrier
	s_branch .LBB0_1249

.LBB0_1254:
	v_add_u32_e32 v140, 0x10000, v177
	v_add_u32_e32 v141, 0x14000, v177
	ds_read_b128 v[132:135], v140
	ds_read_b128 v[136:139], v140 offset:1024
	ds_read_b128 v[186:189], v140 offset:2048
	ds_read_b128 v[190:193], v140 offset:3072
	ds_read_b128 v[194:197], v141
	ds_read_b128 v[198:201], v141 offset:1024
	ds_read_b128 v[202:205], v141 offset:2048
	ds_read_b128 v[206:209], v141 offset:3072
	s_add_i32 s10, s6, s5
	s_add_i32 s11, s5, 0xffffff80
	s_cmp_eq_u32 s4, 12
	s_cselect_b64 vcc, -1, 0
	s_and_b64 s[8:9], vcc, exec
	v_cndmask_b32_e32 v140, v128, v182, vcc
	s_cselect_b32 s7, 0, s5
	v_cndmask_b32_e32 v141, v130, v184, vcc
	v_cndmask_b32_e32 v142, v129, v183, vcc
	s_mov_b32 m0, s57
	ds_read_b128 v[210:213], v178
	ds_read_b128 v[214:217], v178 offset:1024
	ds_read_b128 v[218:221], v178 offset:2048
	ds_read_b128 v[222:225], v178 offset:3072
	ds_read_b128 v[226:229], v178 offset:4096
	ds_read_b128 v[230:233], v178 offset:5120
	ds_read_b128 v[234:237], v178 offset:6144
	ds_read_b128 v[238:241], v178 offset:7168
	buffer_load_dwordx4 v130, s[20:23], s11 offen lds
	s_mov_b32 m0, s58
	s_cselect_b32 s8, s80, s10
	buffer_load_dwordx4 v131, s[20:23], s11 offen lds
	s_waitcnt vmcnt(8)
	s_waitcnt lgkmcnt(0)
	s_barrier
	s_setprio 1
	s_nop 1
	s_waitcnt lgkmcnt(6)
	v_mfma_f32_16x16x128_f8f6f4 v[124:127], v[132:139], v[210:217], v[124:127]
	v_mfma_f32_16x16x128_f8f6f4 v[120:123], v[186:193], v[210:217], v[120:123]
	s_waitcnt lgkmcnt(4)
	v_mfma_f32_16x16x128_f8f6f4 v[108:111], v[132:139], v[218:225], v[108:111]
	v_mfma_f32_16x16x128_f8f6f4 v[104:107], v[186:193], v[218:225], v[104:107]
	s_waitcnt lgkmcnt(2)
	v_mfma_f32_16x16x128_f8f6f4 v[92:95], v[132:139], v[226:233], v[92:95]
	v_mfma_f32_16x16x128_f8f6f4 v[88:91], v[186:193], v[226:233], v[88:91]
	s_waitcnt lgkmcnt(0)
	v_mfma_f32_16x16x128_f8f6f4 v[76:79], v[132:139], v[234:241], v[76:79]
	v_mfma_f32_16x16x128_f8f6f4 v[72:75], v[186:193], v[234:241], v[72:75]
	s_setprio 0
	s_setprio 1
	s_nop 1
	v_mfma_f32_16x16x128_f8f6f4 v[116:119], v[194:201], v[210:217], v[116:119]
	v_mfma_f32_16x16x128_f8f6f4 v[112:115], v[202:209], v[210:217], v[112:115]
	v_mfma_f32_16x16x128_f8f6f4 v[100:103], v[194:201], v[218:225], v[100:103]
	v_mfma_f32_16x16x128_f8f6f4 v[96:99], v[202:209], v[218:225], v[96:99]
	v_mfma_f32_16x16x128_f8f6f4 v[84:87], v[194:201], v[226:233], v[84:87]
	v_mfma_f32_16x16x128_f8f6f4 v[80:83], v[202:209], v[226:233], v[80:83]
	v_mfma_f32_16x16x128_f8f6f4 v[68:71], v[194:201], v[234:241], v[68:71]
	v_mfma_f32_16x16x128_f8f6f4 v[64:67], v[202:209], v[234:241], v[64:67]
	s_setprio 0
	s_barrier
	s_mov_b32 m0, s43
	s_mov_b32 s26, s22
	s_mov_b32 s27, s23
	ds_read_b128 v[210:213], v178 offset:16384
	ds_read_b128 v[214:217], v178 offset:17408
	ds_read_b128 v[218:221], v178 offset:18432
	ds_read_b128 v[222:225], v178 offset:19456
	ds_read_b128 v[226:229], v178 offset:20480
	ds_read_b128 v[230:233], v178 offset:21504
	ds_read_b128 v[234:237], v178 offset:22528
	ds_read_b128 v[238:241], v178 offset:23552
	buffer_load_dwordx4 v155, s[24:27], s8 offen lds
	s_mov_b32 m0, s44
	s_add_i32 s9, s8, 0x4000
	buffer_load_dwordx4 v161, s[24:27], s8 offen lds
	s_mov_b32 m0, s45
	s_nop 0
	buffer_load_dwordx4 v155, s[24:27], s9 offen lds
	s_mov_b32 m0, s46
	s_nop 0
	buffer_load_dwordx4 v161, s[24:27], s9 offen lds
	s_mov_b32 m0, s42
	s_nop 0
	buffer_load_dwordx4 v140, s[20:23], s7 offen lds
	s_mov_b32 m0, s47
	s_nop 0
	buffer_load_dwordx4 v142, s[20:23], s7 offen lds
	s_waitcnt vmcnt(8)
	s_waitcnt lgkmcnt(0)
	s_barrier
	s_setprio 1
	s_nop 1
	s_waitcnt lgkmcnt(6)
	v_mfma_f32_16x16x128_f8f6f4 v[60:63], v[132:139], v[210:217], v[60:63]
	v_mfma_f32_16x16x128_f8f6f4 v[56:59], v[186:193], v[210:217], v[56:59]
	s_waitcnt lgkmcnt(4)
	v_mfma_f32_16x16x128_f8f6f4 v[44:47], v[132:139], v[218:225], v[44:47]
	v_mfma_f32_16x16x128_f8f6f4 v[40:43], v[186:193], v[218:225], v[40:43]
	s_waitcnt lgkmcnt(2)
	v_mfma_f32_16x16x128_f8f6f4 v[28:31], v[132:139], v[226:233], v[28:31]
	v_mfma_f32_16x16x128_f8f6f4 v[24:27], v[186:193], v[226:233], v[24:27]
	s_waitcnt lgkmcnt(0)
	v_mfma_f32_16x16x128_f8f6f4 v[12:15], v[132:139], v[234:241], v[12:15]
	v_mfma_f32_16x16x128_f8f6f4 v[8:11], v[186:193], v[234:241], v[8:11]
	s_setprio 0
	s_setprio 1
	s_nop 1
	v_mfma_f32_16x16x128_f8f6f4 v[52:55], v[194:201], v[210:217], v[52:55]
	v_mfma_f32_16x16x128_f8f6f4 v[48:51], v[202:209], v[210:217], v[48:51]
	v_mfma_f32_16x16x128_f8f6f4 v[36:39], v[194:201], v[218:225], v[36:39]
	v_mfma_f32_16x16x128_f8f6f4 v[32:35], v[202:209], v[218:225], v[32:35]
	v_mfma_f32_16x16x128_f8f6f4 v[20:23], v[194:201], v[226:233], v[20:23]
	v_mfma_f32_16x16x128_f8f6f4 v[16:19], v[202:209], v[226:233], v[16:19]
	v_mfma_f32_16x16x128_f8f6f4 v[4:7], v[194:201], v[234:241], v[4:7]
	v_mfma_f32_16x16x128_f8f6f4 v[0:3], v[202:209], v[234:241], v[0:3]
	s_setprio 0
	s_barrier
	v_add_u32_e32 v143, 0x18000, v177
	ds_read_b128 v[132:135], v143
	ds_read_b128 v[136:139], v143 offset:1024
	ds_read_b128 v[186:189], v143 offset:2048
	ds_read_b128 v[190:193], v143 offset:3072
	v_add_u32_e32 v143, 0x1c000, v177
	ds_read_b128 v[194:197], v143
	ds_read_b128 v[198:201], v143 offset:1024
	ds_read_b128 v[202:205], v143 offset:2048
	ds_read_b128 v[206:209], v143 offset:3072
	s_mov_b32 m0, s48
	ds_read_b128 v[210:213], v178 offset:32768
	ds_read_b128 v[214:217], v178 offset:33792
	ds_read_b128 v[218:221], v178 offset:34816
	ds_read_b128 v[222:225], v178 offset:35840
	ds_read_b128 v[226:229], v178 offset:36864
	ds_read_b128 v[230:233], v178 offset:37888
	ds_read_b128 v[234:237], v178 offset:38912
	ds_read_b128 v[238:241], v178 offset:39936
	v_cndmask_b32_e32 v143, v131, v185, vcc
	buffer_load_dwordx4 v141, s[20:23], s7 offen lds
	s_mov_b32 m0, s49
	s_nop 0
	buffer_load_dwordx4 v143, s[20:23], s7 offen lds
	s_waitcnt vmcnt(8)
	s_waitcnt lgkmcnt(0)
	s_barrier
	s_setprio 1
	s_nop 1
	s_waitcnt lgkmcnt(6)
	v_mfma_f32_16x16x128_f8f6f4 v[124:127], v[132:139], v[210:217], v[124:127]
	v_mfma_f32_16x16x128_f8f6f4 v[120:123], v[186:193], v[210:217], v[120:123]
	s_waitcnt lgkmcnt(4)
	v_mfma_f32_16x16x128_f8f6f4 v[108:111], v[132:139], v[218:225], v[108:111]
	v_mfma_f32_16x16x128_f8f6f4 v[104:107], v[186:193], v[218:225], v[104:107]
	s_waitcnt lgkmcnt(2)
	v_mfma_f32_16x16x128_f8f6f4 v[92:95], v[132:139], v[226:233], v[92:95]
	v_mfma_f32_16x16x128_f8f6f4 v[88:91], v[186:193], v[226:233], v[88:91]
	s_waitcnt lgkmcnt(0)
	v_mfma_f32_16x16x128_f8f6f4 v[76:79], v[132:139], v[234:241], v[76:79]
	v_mfma_f32_16x16x128_f8f6f4 v[72:75], v[186:193], v[234:241], v[72:75]
	s_setprio 0
	s_setprio 1
	s_nop 1
	v_mfma_f32_16x16x128_f8f6f4 v[116:119], v[194:201], v[210:217], v[116:119]
	v_mfma_f32_16x16x128_f8f6f4 v[112:115], v[202:209], v[210:217], v[112:115]
	v_mfma_f32_16x16x128_f8f6f4 v[100:103], v[194:201], v[218:225], v[100:103]
	v_mfma_f32_16x16x128_f8f6f4 v[96:99], v[202:209], v[218:225], v[96:99]
	v_mfma_f32_16x16x128_f8f6f4 v[84:87], v[194:201], v[226:233], v[84:87]
	v_mfma_f32_16x16x128_f8f6f4 v[80:83], v[202:209], v[226:233], v[80:83]
	v_mfma_f32_16x16x128_f8f6f4 v[68:71], v[194:201], v[234:241], v[68:71]
	v_mfma_f32_16x16x128_f8f6f4 v[64:67], v[202:209], v[234:241], v[64:67]
	s_setprio 0
	s_barrier
	s_mov_b32 m0, s51
	s_add_i32 s9, s8, 0x80
	ds_read_b128 v[210:213], v178 offset:49152
	ds_read_b128 v[214:217], v178 offset:50176
	ds_read_b128 v[218:221], v178 offset:51200
	ds_read_b128 v[222:225], v178 offset:52224
	ds_read_b128 v[226:229], v178 offset:53248
	ds_read_b128 v[230:233], v178 offset:54272
	ds_read_b128 v[234:237], v178 offset:55296
	ds_read_b128 v[238:241], v178 offset:56320
	buffer_load_dwordx4 v155, s[24:27], s9 offen lds
	s_mov_b32 m0, s52
	s_add_i32 s8, s8, 0x4080
	buffer_load_dwordx4 v161, s[24:27], s9 offen lds
	s_mov_b32 m0, s55
	s_bitset1_b32 s7, 7
	buffer_load_dwordx4 v155, s[24:27], s8 offen lds
	s_mov_b32 m0, s56
	s_nop 0
	buffer_load_dwordx4 v161, s[24:27], s8 offen lds
	s_mov_b32 m0, s53
	s_nop 0
	buffer_load_dwordx4 v140, s[20:23], s7 offen lds
	s_mov_b32 m0, s54
	s_nop 0
	buffer_load_dwordx4 v142, s[20:23], s7 offen lds
	s_waitcnt vmcnt(8)
	s_waitcnt lgkmcnt(0)
	s_barrier
	s_setprio 1
	s_nop 1
	s_waitcnt lgkmcnt(6)
	v_mfma_f32_16x16x128_f8f6f4 v[60:63], v[132:139], v[210:217], v[60:63]
	v_mfma_f32_16x16x128_f8f6f4 v[56:59], v[186:193], v[210:217], v[56:59]
	s_waitcnt lgkmcnt(4)
	v_mfma_f32_16x16x128_f8f6f4 v[44:47], v[132:139], v[218:225], v[44:47]
	v_mfma_f32_16x16x128_f8f6f4 v[40:43], v[186:193], v[218:225], v[40:43]
	s_waitcnt lgkmcnt(2)
	v_mfma_f32_16x16x128_f8f6f4 v[28:31], v[132:139], v[226:233], v[28:31]
	v_mfma_f32_16x16x128_f8f6f4 v[24:27], v[186:193], v[226:233], v[24:27]
	s_waitcnt lgkmcnt(0)
	v_mfma_f32_16x16x128_f8f6f4 v[12:15], v[132:139], v[234:241], v[12:15]
	v_mfma_f32_16x16x128_f8f6f4 v[8:11], v[186:193], v[234:241], v[8:11]
	s_setprio 0
	s_setprio 1
	s_nop 1
	v_mfma_f32_16x16x128_f8f6f4 v[52:55], v[194:201], v[210:217], v[52:55]
	v_mfma_f32_16x16x128_f8f6f4 v[48:51], v[202:209], v[210:217], v[48:51]
	v_mfma_f32_16x16x128_f8f6f4 v[36:39], v[194:201], v[218:225], v[36:39]
	v_mfma_f32_16x16x128_f8f6f4 v[32:35], v[202:209], v[218:225], v[32:35]
	v_mfma_f32_16x16x128_f8f6f4 v[20:23], v[194:201], v[226:233], v[20:23]
	v_mfma_f32_16x16x128_f8f6f4 v[16:19], v[202:209], v[226:233], v[16:19]
	v_mfma_f32_16x16x128_f8f6f4 v[4:7], v[194:201], v[234:241], v[4:7]
	v_mfma_f32_16x16x128_f8f6f4 v[0:3], v[202:209], v[234:241], v[0:3]
	s_setprio 0
	s_barrier
	s_add_i32 s4, s4, 2
	s_addk_i32 s5, 0x100
	s_cmp_gt_u32 s4, 13
	s_cbranch_scc0 .LBB0_1254
	s_and_b64 vcc, exec, s[38:39]
	s_cbranch_vccz .LBB0_1257
	s_barrier
.LBB0_1257:
	v_ashrrev_i32_e32 v147, 31, v146
	v_readlane_b32 s4, v253, 45
	v_lshlrev_b64 v[128:129], 13, v[146:147]
	v_readlane_b32 s16, v253, 57
	v_readlane_b32 s17, v253, 58
	v_readlane_b32 s14, v253, 55
	v_readlane_b32 s15, v253, 56
	v_lshl_add_u64 v[128:129], s[16:17], 0, v[128:129]
	v_cmp_gt_i32_e64 s[16:17], s81, v168
	v_readlane_b32 s12, v253, 53
	v_readlane_b32 s13, v253, 54
	v_cndmask_b32_e64 v144, 0, v168, s[16:17]
	v_cmp_gt_i32_e64 s[14:15], s81, v170
	v_readlane_b32 s10, v253, 51
	v_readlane_b32 s11, v253, 52
	v_lshlrev_b32_e32 v163, 2, v144
	v_cndmask_b32_e64 v144, 0, v170, s[14:15]
	v_cmp_gt_i32_e64 s[12:13], s81, v171
	v_readlane_b32 s8, v253, 49
	v_readlane_b32 s9, v253, 50
	v_lshlrev_b32_e32 v150, 2, v144
	v_cndmask_b32_e64 v144, 0, v171, s[12:13]
	v_cmp_gt_i32_e64 s[10:11], s81, v172
	v_lshl_or_b32 v148, s1, 8, v169
	s_ashr_i32 s1, s0, 31
	v_lshlrev_b64 v[164:165], 18, v[146:147]
	v_lshlrev_b32_e32 v152, 2, v144
	v_cndmask_b32_e64 v144, 0, v172, s[10:11]
	v_cmp_gt_i32_e64 s[8:9], s81, v173
	v_lshl_add_u64 v[146:147], s[34:35], 0, v[164:165]
	s_lshl_b64 s[0:1], s[0:1], 2
	v_lshlrev_b32_e32 v154, 2, v144
	v_cndmask_b32_e64 v144, 0, v173, s[8:9]
	v_readlane_b32 s5, v253, 46
	v_readlane_b32 s6, v253, 47
	v_readlane_b32 s7, v253, 48
	v_ashrrev_i32_e32 v149, 31, v148
	v_lshl_add_u64 v[146:147], v[146:147], 0, s[0:1]
	v_lshlrev_b64 v[192:193], 2, v[144:145]
	s_nop 15
	s_nop 15
	v_lshl_add_u64 v[132:133], v[148:149], 2, v[128:129]
	v_readfirstlane_b32 s4, v146
	v_readfirstlane_b32 s5, v147
	v_lshl_add_u64 v[186:187], v[146:147], 0, v[192:193]
	v_cmp_gt_i32_e64 s[6:7], s81, v174
	global_load_dwordx4 v[136:139], v[132:133], off offset:16
	global_load_dwordx4 v[140:143], v[132:133], off
	global_load_dwordx4 v[128:131], v[132:133], off offset:48
	s_nop 0
	global_load_dwordx4 v[132:135], v[132:133], off offset:32
	v_cndmask_b32_e64 v144, 0, v174, s[6:7]
	global_load_dword v162, v163, s[4:5]
	global_load_dword v191, v150, s[4:5]
	global_load_dword v190, v152, s[4:5]
	global_load_dword v188, v[186:187], off
	global_load_dword v189, v154, s[4:5]
	v_cmp_gt_i32_e64 s[4:5], s81, v175
	v_lshlrev_b64 v[194:195], 2, v[144:145]
	v_cmp_gt_i32_e32 vcc, s81, v176
	v_cndmask_b32_e64 v144, 0, v175, s[4:5]
	v_lshlrev_b64 v[196:197], 2, v[144:145]
	v_lshl_add_u64 v[186:187], v[146:147], 0, v[194:195]
	v_lshl_add_u64 v[198:199], v[146:147], 0, v[196:197]
	v_cndmask_b32_e32 v144, 0, v176, vcc
	v_lshl_add_u64 v[164:165], s[30:31], 0, v[164:165]
	global_load_dword v187, v[186:187], off
	v_lshl_add_u64 v[164:165], v[164:165], 0, s[0:1]
	global_load_dword v186, v[198:199], off
	v_lshlrev_b64 v[198:199], 2, v[144:145]
	v_lshl_add_u64 v[146:147], v[146:147], 0, v[198:199]
	v_readfirstlane_b32 s0, v164
	v_readfirstlane_b32 s1, v165
	v_lshl_add_u64 v[192:193], v[164:165], 0, v[192:193]
	global_load_dword v147, v[146:147], off
	s_nop 2
	global_load_dword v160, v150, s[0:1]
	global_load_dword v158, v152, s[0:1]
	global_load_dword v156, v154, s[0:1]
	v_readlane_b32 s18, v253, 59
	global_load_dword v154, v[192:193], off
	v_lshl_add_u64 v[192:193], v[164:165], 0, v[194:195]
	global_load_dword v152, v[192:193], off
	v_lshl_add_u64 v[192:193], v[164:165], 0, v[196:197]
	global_load_dword v150, v[192:193], off
	v_lshl_add_u64 v[192:193], v[164:165], 0, v[198:199]
	global_load_dword v146, v[192:193], off
	v_readlane_b32 s19, v253, 60
	s_waitcnt vmcnt(0)
	v_cndmask_b32_e64 v162, -1, v162, s[16:17]
	v_cmp_lt_i32_e64 s[0:1], -1, v162
	s_and_saveexec_b64 s[16:17], s[0:1]
	s_cbranch_execz .LBB0_1259
	v_readfirstlane_b32 s0, v164
	v_readfirstlane_b32 s1, v165
	v_pk_fma_f32 v[124:125], v[124:125], s[40:41], v[140:141] op_sel_hi:[1,0,1]
	v_pk_fma_f32 v[120:121], v[120:121], s[40:41], v[136:137] op_sel_hi:[1,0,1]
	v_pk_fma_f32 v[116:117], v[116:117], s[40:41], v[132:133] op_sel_hi:[1,0,1]
	v_pk_fma_f32 v[112:113], v[112:113], s[40:41], v[128:129] op_sel_hi:[1,0,1]
	global_load_dword v144, v163, s[0:1]
	v_pk_fma_f32 v[126:127], v[126:127], s[40:41], v[142:143] op_sel_hi:[1,0,1]
	v_pk_fma_f32 v[122:123], v[122:123], s[40:41], v[138:139] op_sel_hi:[1,0,1]
	v_pk_fma_f32 v[118:119], v[118:119], s[40:41], v[134:135] op_sel_hi:[1,0,1]
	v_pk_fma_f32 v[114:115], v[114:115], s[40:41], v[130:131] op_sel_hi:[1,0,1]
	v_mov_b32_e32 v163, v145
	v_lshlrev_b64 v[162:163], 11, v[162:163]
	s_waitcnt vmcnt(0)
	v_pk_mul_f32 v[124:125], v[124:125], v[144:145] op_sel_hi:[1,0]
	v_pk_mul_f32 v[120:121], v[120:121], v[144:145] op_sel_hi:[1,0]
	v_pk_mul_f32 v[116:117], v[116:117], v[144:145] op_sel_hi:[1,0]
	v_pk_mul_f32 v[112:113], v[112:113], v[144:145] op_sel_hi:[1,0]
	v_mul_f32_e32 v124, 0x41800000, v124
	v_mul_f32_e32 v125, 0x41800000, v125
	v_mul_f32_e32 v120, 0x41800000, v120
	v_mul_f32_e32 v121, 0x41800000, v121
	v_mul_f32_e32 v116, 0x41800000, v116
	v_mul_f32_e32 v117, 0x41800000, v117
	v_mul_f32_e32 v112, 0x41800000, v112
	v_mul_f32_e32 v113, 0x41800000, v113
	v_med3_f32 v124, v124, s75, v180
	v_med3_f32 v125, v125, s75, v180
	v_med3_f32 v120, v120, s75, v180
	v_med3_f32 v121, v121, s75, v180
	v_med3_f32 v116, v116, s75, v180
	v_med3_f32 v117, v117, s75, v180
	v_med3_f32 v112, v112, s75, v180
	v_med3_f32 v113, v113, s75, v180
	v_cvt_pk_fp8_f32 v200, v124, v125
	v_cvt_pk_fp8_f32 v201, v120, v121
	v_pk_mul_f32 v[126:127], v[126:127], v[144:145] op_sel_hi:[1,0]
	v_pk_mul_f32 v[122:123], v[122:123], v[144:145] op_sel_hi:[1,0]
	v_cvt_pk_fp8_f32 v202, v116, v117
	v_cvt_pk_fp8_f32 v203, v112, v113
	v_pk_mul_f32 v[118:119], v[118:119], v[144:145] op_sel_hi:[1,0]
	v_pk_mul_f32 v[114:115], v[114:115], v[144:145] op_sel_hi:[1,0]
	v_mul_f32_e32 v126, 0x41800000, v126
	v_mul_f32_e32 v127, 0x41800000, v127
	v_mul_f32_e32 v122, 0x41800000, v122
	v_mul_f32_e32 v123, 0x41800000, v123
	v_mul_f32_e32 v118, 0x41800000, v118
	v_mul_f32_e32 v119, 0x41800000, v119
	v_mul_f32_e32 v114, 0x41800000, v114
	v_mul_f32_e32 v115, 0x41800000, v115
	v_med3_f32 v126, v126, s75, v180
	v_med3_f32 v127, v127, s75, v180
	v_med3_f32 v122, v122, s75, v180
	v_med3_f32 v123, v123, s75, v180
	v_med3_f32 v118, v118, s75, v180
	v_med3_f32 v119, v119, s75, v180
	v_med3_f32 v114, v114, s75, v180
	v_med3_f32 v115, v115, s75, v180
	v_cvt_pk_fp8_f32 v200, v126, v127 op_sel:[0,0,1]
	v_cvt_pk_fp8_f32 v201, v122, v123 op_sel:[0,0,1]
	v_cvt_pk_fp8_f32 v202, v118, v119 op_sel:[0,0,1]
	v_cvt_pk_fp8_f32 v203, v114, v115 op_sel:[0,0,1]
	v_lshl_add_u64 v[112:113], s[36:37], 0, v[162:163]
	v_lshl_add_u64 v[112:113], v[112:113], 0, v[148:149]
	global_store_dwordx4 v[112:113], v[200:203], off
.LBB0_1259:
	s_or_b64 exec, exec, s[16:17]
	v_cndmask_b32_e64 v144, -1, v191, s[14:15]
	v_cmp_lt_i32_e64 s[0:1], -1, v144
	s_and_saveexec_b64 s[14:15], s[0:1]
	s_cbranch_execz .LBB0_1261
	v_pk_fma_f32 v[108:109], v[108:109], s[40:41], v[140:141] op_sel_hi:[1,0,1]
	v_pk_fma_f32 v[110:111], v[110:111], s[40:41], v[142:143] op_sel_hi:[1,0,1]
	v_pk_mul_f32 v[108:109], v[108:109], v[160:161] op_sel_hi:[1,0]
	v_pk_mul_f32 v[110:111], v[110:111], v[160:161] op_sel_hi:[1,0]
	v_mul_f32_e32 v108, 0x41800000, v108
	v_mul_f32_e32 v109, 0x41800000, v109
	v_med3_f32 v114, v108, s75, v180
	v_med3_f32 v109, v109, s75, v180
	v_cvt_pk_fp8_f32 v204, v114, v109
	v_pk_fma_f32 v[104:105], v[104:105], s[40:41], v[136:137] op_sel_hi:[1,0,1]
	v_mul_f32_e32 v110, 0x41800000, v110
	v_pk_mul_f32 v[104:105], v[104:105], v[160:161] op_sel_hi:[1,0]
	v_mul_f32_e32 v109, 0x41800000, v111
	v_med3_f32 v110, v110, s75, v180
	v_med3_f32 v109, v109, s75, v180
	v_mul_f32_e32 v104, 0x41800000, v104
	v_mul_f32_e32 v105, 0x41800000, v105
	v_cvt_pk_fp8_f32 v204, v110, v109 op_sel:[0,0,1]
	v_med3_f32 v104, v104, s75, v180
	v_med3_f32 v105, v105, s75, v180
	v_pk_fma_f32 v[106:107], v[106:107], s[40:41], v[138:139] op_sel_hi:[1,0,1]
	v_cvt_pk_fp8_f32 v205, v104, v105
	v_pk_mul_f32 v[106:107], v[106:107], v[160:161] op_sel_hi:[1,0]
	v_pk_fma_f32 v[100:101], v[100:101], s[40:41], v[132:133] op_sel_hi:[1,0,1]
	v_mul_f32_e32 v106, 0x41800000, v106
	v_mul_f32_e32 v104, 0x41800000, v107
	v_pk_mul_f32 v[100:101], v[100:101], v[160:161] op_sel_hi:[1,0]
	v_med3_f32 v105, v106, s75, v180
	v_med3_f32 v104, v104, s75, v180
	v_mul_f32_e32 v100, 0x41800000, v100
	v_mul_f32_e32 v101, 0x41800000, v101
	v_cvt_pk_fp8_f32 v205, v105, v104 op_sel:[0,0,1]
	v_med3_f32 v104, v100, s75, v180
	v_med3_f32 v101, v101, s75, v180
	v_pk_fma_f32 v[102:103], v[102:103], s[40:41], v[134:135] op_sel_hi:[1,0,1]
	v_cvt_pk_fp8_f32 v206, v104, v101
	v_pk_mul_f32 v[102:103], v[102:103], v[160:161] op_sel_hi:[1,0]
	v_pk_fma_f32 v[96:97], v[96:97], s[40:41], v[128:129] op_sel_hi:[1,0,1]
	v_mul_f32_e32 v102, 0x41800000, v102
	v_pk_mul_f32 v[96:97], v[96:97], v[160:161] op_sel_hi:[1,0]
	v_mul_f32_e32 v101, 0x41800000, v103
	v_med3_f32 v102, v102, s75, v180
	v_med3_f32 v101, v101, s75, v180
	v_mul_f32_e32 v96, 0x41800000, v96
	v_mul_f32_e32 v97, 0x41800000, v97
	v_cvt_pk_fp8_f32 v206, v102, v101 op_sel:[0,0,1]
	v_med3_f32 v96, v96, s75, v180
	v_med3_f32 v97, v97, s75, v180
	v_pk_fma_f32 v[98:99], v[98:99], s[40:41], v[130:131] op_sel_hi:[1,0,1]
	v_cvt_pk_fp8_f32 v207, v96, v97
	v_pk_mul_f32 v[98:99], v[98:99], v[160:161] op_sel_hi:[1,0]
	v_lshlrev_b64 v[112:113], 11, v[144:145]
	v_mul_f32_e32 v98, 0x41800000, v98
	v_mul_f32_e32 v96, 0x41800000, v99
	v_med3_f32 v97, v98, s75, v180
	v_med3_f32 v96, v96, s75, v180
	v_cvt_pk_fp8_f32 v207, v97, v96 op_sel:[0,0,1]
	v_lshl_add_u64 v[96:97], s[36:37], 0, v[112:113]
	v_lshl_add_u64 v[96:97], v[96:97], 0, v[148:149]
	global_store_dwordx4 v[96:97], v[204:207], off
.LBB0_1261:
	s_or_b64 exec, exec, s[14:15]
	v_cndmask_b32_e64 v144, -1, v190, s[12:13]
	v_cmp_lt_i32_e64 s[0:1], -1, v144
	s_and_saveexec_b64 s[12:13], s[0:1]
	s_cbranch_execz .LBB0_1263
	v_pk_fma_f32 v[92:93], v[92:93], s[40:41], v[140:141] op_sel_hi:[1,0,1]
	v_pk_fma_f32 v[94:95], v[94:95], s[40:41], v[142:143] op_sel_hi:[1,0,1]
	v_pk_mul_f32 v[92:93], v[92:93], v[158:159] op_sel_hi:[1,0]
	v_pk_mul_f32 v[94:95], v[94:95], v[158:159] op_sel_hi:[1,0]
	v_mul_f32_e32 v92, 0x41800000, v92
	v_mul_f32_e32 v93, 0x41800000, v93
	v_med3_f32 v98, v92, s75, v180
	v_med3_f32 v93, v93, s75, v180
	v_cvt_pk_fp8_f32 v208, v98, v93
	v_pk_fma_f32 v[88:89], v[88:89], s[40:41], v[136:137] op_sel_hi:[1,0,1]
	v_mul_f32_e32 v94, 0x41800000, v94
	v_pk_mul_f32 v[88:89], v[88:89], v[158:159] op_sel_hi:[1,0]
	v_mul_f32_e32 v93, 0x41800000, v95
	v_med3_f32 v94, v94, s75, v180
	v_med3_f32 v93, v93, s75, v180
	v_mul_f32_e32 v88, 0x41800000, v88
	v_mul_f32_e32 v89, 0x41800000, v89
	v_cvt_pk_fp8_f32 v208, v94, v93 op_sel:[0,0,1]
	v_med3_f32 v88, v88, s75, v180
	v_med3_f32 v89, v89, s75, v180
	v_pk_fma_f32 v[90:91], v[90:91], s[40:41], v[138:139] op_sel_hi:[1,0,1]
	v_cvt_pk_fp8_f32 v209, v88, v89
	v_pk_mul_f32 v[90:91], v[90:91], v[158:159] op_sel_hi:[1,0]
	v_pk_fma_f32 v[84:85], v[84:85], s[40:41], v[132:133] op_sel_hi:[1,0,1]
	v_mul_f32_e32 v90, 0x41800000, v90
	v_mul_f32_e32 v88, 0x41800000, v91
	v_pk_mul_f32 v[84:85], v[84:85], v[158:159] op_sel_hi:[1,0]
	v_med3_f32 v89, v90, s75, v180
	v_med3_f32 v88, v88, s75, v180
	v_mul_f32_e32 v84, 0x41800000, v84
	v_mul_f32_e32 v85, 0x41800000, v85
	v_cvt_pk_fp8_f32 v209, v89, v88 op_sel:[0,0,1]
	v_med3_f32 v88, v84, s75, v180
	v_med3_f32 v85, v85, s75, v180
	v_pk_fma_f32 v[86:87], v[86:87], s[40:41], v[134:135] op_sel_hi:[1,0,1]
	v_cvt_pk_fp8_f32 v210, v88, v85
	v_pk_mul_f32 v[86:87], v[86:87], v[158:159] op_sel_hi:[1,0]
	v_pk_fma_f32 v[80:81], v[80:81], s[40:41], v[128:129] op_sel_hi:[1,0,1]
	v_mul_f32_e32 v86, 0x41800000, v86
	v_pk_mul_f32 v[80:81], v[80:81], v[158:159] op_sel_hi:[1,0]
	v_mul_f32_e32 v85, 0x41800000, v87
	v_med3_f32 v86, v86, s75, v180
	v_med3_f32 v85, v85, s75, v180
	v_mul_f32_e32 v80, 0x41800000, v80
	v_mul_f32_e32 v81, 0x41800000, v81
	v_cvt_pk_fp8_f32 v210, v86, v85 op_sel:[0,0,1]
	v_med3_f32 v80, v80, s75, v180
	v_med3_f32 v81, v81, s75, v180
	v_pk_fma_f32 v[82:83], v[82:83], s[40:41], v[130:131] op_sel_hi:[1,0,1]
	v_cvt_pk_fp8_f32 v211, v80, v81
	v_pk_mul_f32 v[82:83], v[82:83], v[158:159] op_sel_hi:[1,0]
	v_lshlrev_b64 v[96:97], 11, v[144:145]
	v_mul_f32_e32 v82, 0x41800000, v82
	v_mul_f32_e32 v80, 0x41800000, v83
	v_med3_f32 v81, v82, s75, v180
	v_med3_f32 v80, v80, s75, v180
	v_cvt_pk_fp8_f32 v211, v81, v80 op_sel:[0,0,1]
	v_lshl_add_u64 v[80:81], s[36:37], 0, v[96:97]
	v_lshl_add_u64 v[80:81], v[80:81], 0, v[148:149]
	global_store_dwordx4 v[80:81], v[208:211], off
.LBB0_1263:
	s_or_b64 exec, exec, s[12:13]
	v_cndmask_b32_e64 v144, -1, v189, s[10:11]
	v_cmp_lt_i32_e64 s[0:1], -1, v144
	s_and_saveexec_b64 s[10:11], s[0:1]
	s_cbranch_execz .LBB0_1265
	v_pk_fma_f32 v[76:77], v[76:77], s[40:41], v[140:141] op_sel_hi:[1,0,1]
	v_pk_fma_f32 v[78:79], v[78:79], s[40:41], v[142:143] op_sel_hi:[1,0,1]
	v_pk_mul_f32 v[76:77], v[76:77], v[156:157] op_sel_hi:[1,0]
	v_pk_mul_f32 v[78:79], v[78:79], v[156:157] op_sel_hi:[1,0]
	v_mul_f32_e32 v76, 0x41800000, v76
	v_mul_f32_e32 v77, 0x41800000, v77
	v_med3_f32 v82, v76, s75, v180
	v_med3_f32 v77, v77, s75, v180
	v_cvt_pk_fp8_f32 v212, v82, v77
	v_pk_fma_f32 v[72:73], v[72:73], s[40:41], v[136:137] op_sel_hi:[1,0,1]
	v_mul_f32_e32 v78, 0x41800000, v78
	v_pk_mul_f32 v[72:73], v[72:73], v[156:157] op_sel_hi:[1,0]
	v_mul_f32_e32 v77, 0x41800000, v79
	v_med3_f32 v78, v78, s75, v180
	v_med3_f32 v77, v77, s75, v180
	v_mul_f32_e32 v72, 0x41800000, v72
	v_mul_f32_e32 v73, 0x41800000, v73
	v_cvt_pk_fp8_f32 v212, v78, v77 op_sel:[0,0,1]
	v_med3_f32 v72, v72, s75, v180
	v_med3_f32 v73, v73, s75, v180
	v_pk_fma_f32 v[74:75], v[74:75], s[40:41], v[138:139] op_sel_hi:[1,0,1]
	v_cvt_pk_fp8_f32 v213, v72, v73
	v_pk_mul_f32 v[74:75], v[74:75], v[156:157] op_sel_hi:[1,0]
	v_pk_fma_f32 v[68:69], v[68:69], s[40:41], v[132:133] op_sel_hi:[1,0,1]
	v_mul_f32_e32 v74, 0x41800000, v74
	v_mul_f32_e32 v72, 0x41800000, v75
	v_pk_mul_f32 v[68:69], v[68:69], v[156:157] op_sel_hi:[1,0]
	v_med3_f32 v73, v74, s75, v180
	v_med3_f32 v72, v72, s75, v180
	v_mul_f32_e32 v68, 0x41800000, v68
	v_mul_f32_e32 v69, 0x41800000, v69
	v_cvt_pk_fp8_f32 v213, v73, v72 op_sel:[0,0,1]
	v_med3_f32 v72, v68, s75, v180
	v_med3_f32 v69, v69, s75, v180
	v_pk_fma_f32 v[70:71], v[70:71], s[40:41], v[134:135] op_sel_hi:[1,0,1]
	v_cvt_pk_fp8_f32 v214, v72, v69
	v_pk_mul_f32 v[70:71], v[70:71], v[156:157] op_sel_hi:[1,0]
	v_pk_fma_f32 v[64:65], v[64:65], s[40:41], v[128:129] op_sel_hi:[1,0,1]
	v_mul_f32_e32 v70, 0x41800000, v70
	v_pk_mul_f32 v[64:65], v[64:65], v[156:157] op_sel_hi:[1,0]
	v_mul_f32_e32 v69, 0x41800000, v71
	v_med3_f32 v70, v70, s75, v180
	v_med3_f32 v69, v69, s75, v180
	v_mul_f32_e32 v64, 0x41800000, v64
	v_mul_f32_e32 v65, 0x41800000, v65
	v_cvt_pk_fp8_f32 v214, v70, v69 op_sel:[0,0,1]
	v_med3_f32 v64, v64, s75, v180
	v_med3_f32 v65, v65, s75, v180
	v_pk_fma_f32 v[66:67], v[66:67], s[40:41], v[130:131] op_sel_hi:[1,0,1]
	v_cvt_pk_fp8_f32 v215, v64, v65
	v_pk_mul_f32 v[66:67], v[66:67], v[156:157] op_sel_hi:[1,0]
	v_lshlrev_b64 v[80:81], 11, v[144:145]
	v_mul_f32_e32 v66, 0x41800000, v66
	v_mul_f32_e32 v64, 0x41800000, v67
	v_med3_f32 v65, v66, s75, v180
	v_med3_f32 v64, v64, s75, v180
	v_cvt_pk_fp8_f32 v215, v65, v64 op_sel:[0,0,1]
	v_lshl_add_u64 v[64:65], s[36:37], 0, v[80:81]
	v_lshl_add_u64 v[64:65], v[64:65], 0, v[148:149]
	global_store_dwordx4 v[64:65], v[212:215], off
.LBB0_1265:
	s_or_b64 exec, exec, s[10:11]
	v_cndmask_b32_e64 v144, -1, v188, s[8:9]
	v_cmp_lt_i32_e64 s[0:1], -1, v144
	s_and_saveexec_b64 s[8:9], s[0:1]
	s_cbranch_execz .LBB0_1267
	v_pk_fma_f32 v[60:61], v[60:61], s[40:41], v[140:141] op_sel_hi:[1,0,1]
	v_pk_fma_f32 v[62:63], v[62:63], s[40:41], v[142:143] op_sel_hi:[1,0,1]
	v_pk_mul_f32 v[60:61], v[60:61], v[154:155] op_sel_hi:[1,0]
	v_pk_mul_f32 v[62:63], v[62:63], v[154:155] op_sel_hi:[1,0]
	v_mul_f32_e32 v60, 0x41800000, v60
	v_mul_f32_e32 v61, 0x41800000, v61
	v_med3_f32 v66, v60, s75, v180
	v_med3_f32 v61, v61, s75, v180
	v_cvt_pk_fp8_f32 v216, v66, v61
	v_pk_fma_f32 v[56:57], v[56:57], s[40:41], v[136:137] op_sel_hi:[1,0,1]
	v_mul_f32_e32 v62, 0x41800000, v62
	v_pk_mul_f32 v[56:57], v[56:57], v[154:155] op_sel_hi:[1,0]
	v_mul_f32_e32 v61, 0x41800000, v63
	v_med3_f32 v62, v62, s75, v180
	v_med3_f32 v61, v61, s75, v180
	v_mul_f32_e32 v56, 0x41800000, v56
	v_mul_f32_e32 v57, 0x41800000, v57
	v_cvt_pk_fp8_f32 v216, v62, v61 op_sel:[0,0,1]
	v_med3_f32 v56, v56, s75, v180
	v_med3_f32 v57, v57, s75, v180
	v_pk_fma_f32 v[58:59], v[58:59], s[40:41], v[138:139] op_sel_hi:[1,0,1]
	v_cvt_pk_fp8_f32 v217, v56, v57
	v_pk_mul_f32 v[58:59], v[58:59], v[154:155] op_sel_hi:[1,0]
	v_pk_fma_f32 v[52:53], v[52:53], s[40:41], v[132:133] op_sel_hi:[1,0,1]
	v_mul_f32_e32 v58, 0x41800000, v58
	v_mul_f32_e32 v56, 0x41800000, v59
	v_pk_mul_f32 v[52:53], v[52:53], v[154:155] op_sel_hi:[1,0]
	v_med3_f32 v57, v58, s75, v180
	v_med3_f32 v56, v56, s75, v180
	v_mul_f32_e32 v52, 0x41800000, v52
	v_mul_f32_e32 v53, 0x41800000, v53
	v_cvt_pk_fp8_f32 v217, v57, v56 op_sel:[0,0,1]
	v_med3_f32 v56, v52, s75, v180
	v_med3_f32 v53, v53, s75, v180
	v_pk_fma_f32 v[54:55], v[54:55], s[40:41], v[134:135] op_sel_hi:[1,0,1]
	v_cvt_pk_fp8_f32 v218, v56, v53
	v_pk_mul_f32 v[54:55], v[54:55], v[154:155] op_sel_hi:[1,0]
	v_pk_fma_f32 v[48:49], v[48:49], s[40:41], v[128:129] op_sel_hi:[1,0,1]
	v_mul_f32_e32 v54, 0x41800000, v54
	v_pk_mul_f32 v[48:49], v[48:49], v[154:155] op_sel_hi:[1,0]
	v_mul_f32_e32 v53, 0x41800000, v55
	v_med3_f32 v54, v54, s75, v180
	v_med3_f32 v53, v53, s75, v180
	v_mul_f32_e32 v48, 0x41800000, v48
	v_mul_f32_e32 v49, 0x41800000, v49
	v_cvt_pk_fp8_f32 v218, v54, v53 op_sel:[0,0,1]
	v_med3_f32 v48, v48, s75, v180
	v_med3_f32 v49, v49, s75, v180
	v_pk_fma_f32 v[50:51], v[50:51], s[40:41], v[130:131] op_sel_hi:[1,0,1]
	v_cvt_pk_fp8_f32 v219, v48, v49
	v_pk_mul_f32 v[50:51], v[50:51], v[154:155] op_sel_hi:[1,0]
	v_lshlrev_b64 v[64:65], 11, v[144:145]
	v_mul_f32_e32 v50, 0x41800000, v50
	v_mul_f32_e32 v48, 0x41800000, v51
	v_med3_f32 v49, v50, s75, v180
	v_med3_f32 v48, v48, s75, v180
	v_cvt_pk_fp8_f32 v219, v49, v48 op_sel:[0,0,1]
	v_lshl_add_u64 v[48:49], s[36:37], 0, v[64:65]
	v_lshl_add_u64 v[48:49], v[48:49], 0, v[148:149]
	global_store_dwordx4 v[48:49], v[216:219], off
.LBB0_1267:
	s_or_b64 exec, exec, s[8:9]
	v_cndmask_b32_e64 v144, -1, v187, s[6:7]
	v_cmp_lt_i32_e64 s[0:1], -1, v144
	s_and_saveexec_b64 s[6:7], s[0:1]
	s_cbranch_execz .LBB0_1269
	v_pk_fma_f32 v[44:45], v[44:45], s[40:41], v[140:141] op_sel_hi:[1,0,1]
	v_pk_fma_f32 v[46:47], v[46:47], s[40:41], v[142:143] op_sel_hi:[1,0,1]
	v_pk_mul_f32 v[44:45], v[44:45], v[152:153] op_sel_hi:[1,0]
	v_pk_mul_f32 v[46:47], v[46:47], v[152:153] op_sel_hi:[1,0]
	v_mul_f32_e32 v44, 0x41800000, v44
	v_mul_f32_e32 v45, 0x41800000, v45
	v_med3_f32 v50, v44, s75, v180
	v_med3_f32 v45, v45, s75, v180
	v_cvt_pk_fp8_f32 v220, v50, v45
	v_pk_fma_f32 v[40:41], v[40:41], s[40:41], v[136:137] op_sel_hi:[1,0,1]
	v_mul_f32_e32 v46, 0x41800000, v46
	v_pk_mul_f32 v[40:41], v[40:41], v[152:153] op_sel_hi:[1,0]
	v_mul_f32_e32 v45, 0x41800000, v47
	v_med3_f32 v46, v46, s75, v180
	v_med3_f32 v45, v45, s75, v180
	v_mul_f32_e32 v40, 0x41800000, v40
	v_mul_f32_e32 v41, 0x41800000, v41
	v_cvt_pk_fp8_f32 v220, v46, v45 op_sel:[0,0,1]
	v_med3_f32 v40, v40, s75, v180
	v_med3_f32 v41, v41, s75, v180
	v_pk_fma_f32 v[42:43], v[42:43], s[40:41], v[138:139] op_sel_hi:[1,0,1]
	v_cvt_pk_fp8_f32 v221, v40, v41
	v_pk_mul_f32 v[42:43], v[42:43], v[152:153] op_sel_hi:[1,0]
	v_pk_fma_f32 v[36:37], v[36:37], s[40:41], v[132:133] op_sel_hi:[1,0,1]
	v_mul_f32_e32 v42, 0x41800000, v42
	v_mul_f32_e32 v40, 0x41800000, v43
	v_pk_mul_f32 v[36:37], v[36:37], v[152:153] op_sel_hi:[1,0]
	v_med3_f32 v41, v42, s75, v180
	v_med3_f32 v40, v40, s75, v180
	v_mul_f32_e32 v36, 0x41800000, v36
	v_mul_f32_e32 v37, 0x41800000, v37
	v_cvt_pk_fp8_f32 v221, v41, v40 op_sel:[0,0,1]
	v_med3_f32 v40, v36, s75, v180
	v_med3_f32 v37, v37, s75, v180
	v_pk_fma_f32 v[38:39], v[38:39], s[40:41], v[134:135] op_sel_hi:[1,0,1]
	v_cvt_pk_fp8_f32 v222, v40, v37
	v_pk_mul_f32 v[38:39], v[38:39], v[152:153] op_sel_hi:[1,0]
	v_pk_fma_f32 v[32:33], v[32:33], s[40:41], v[128:129] op_sel_hi:[1,0,1]
	v_mul_f32_e32 v38, 0x41800000, v38
	v_pk_mul_f32 v[32:33], v[32:33], v[152:153] op_sel_hi:[1,0]
	v_mul_f32_e32 v37, 0x41800000, v39
	v_med3_f32 v38, v38, s75, v180
	v_med3_f32 v37, v37, s75, v180
	v_mul_f32_e32 v32, 0x41800000, v32
	v_mul_f32_e32 v33, 0x41800000, v33
	v_cvt_pk_fp8_f32 v222, v38, v37 op_sel:[0,0,1]
	v_med3_f32 v32, v32, s75, v180
	v_med3_f32 v33, v33, s75, v180
	v_pk_fma_f32 v[34:35], v[34:35], s[40:41], v[130:131] op_sel_hi:[1,0,1]
	v_cvt_pk_fp8_f32 v223, v32, v33
	v_pk_mul_f32 v[34:35], v[34:35], v[152:153] op_sel_hi:[1,0]
	v_lshlrev_b64 v[48:49], 11, v[144:145]
	v_mul_f32_e32 v34, 0x41800000, v34
	v_mul_f32_e32 v32, 0x41800000, v35
	v_med3_f32 v33, v34, s75, v180
	v_med3_f32 v32, v32, s75, v180
	v_cvt_pk_fp8_f32 v223, v33, v32 op_sel:[0,0,1]
	v_lshl_add_u64 v[32:33], s[36:37], 0, v[48:49]
	v_lshl_add_u64 v[32:33], v[32:33], 0, v[148:149]
	global_store_dwordx4 v[32:33], v[220:223], off
.LBB0_1269:
	s_or_b64 exec, exec, s[6:7]
	v_cndmask_b32_e64 v144, -1, v186, s[4:5]
	v_cmp_lt_i32_e64 s[0:1], -1, v144
	s_and_saveexec_b64 s[4:5], s[0:1]
	s_cbranch_execz .LBB0_1271
	v_pk_fma_f32 v[28:29], v[28:29], s[40:41], v[140:141] op_sel_hi:[1,0,1]
	v_pk_fma_f32 v[30:31], v[30:31], s[40:41], v[142:143] op_sel_hi:[1,0,1]
	v_pk_mul_f32 v[28:29], v[28:29], v[150:151] op_sel_hi:[1,0]
	v_pk_mul_f32 v[30:31], v[30:31], v[150:151] op_sel_hi:[1,0]
	v_mul_f32_e32 v28, 0x41800000, v28
	v_mul_f32_e32 v29, 0x41800000, v29
	v_med3_f32 v34, v28, s75, v180
	v_med3_f32 v29, v29, s75, v180
	v_cvt_pk_fp8_f32 v224, v34, v29
	v_pk_fma_f32 v[24:25], v[24:25], s[40:41], v[136:137] op_sel_hi:[1,0,1]
	v_mul_f32_e32 v30, 0x41800000, v30
	v_pk_mul_f32 v[24:25], v[24:25], v[150:151] op_sel_hi:[1,0]
	v_mul_f32_e32 v29, 0x41800000, v31
	v_med3_f32 v30, v30, s75, v180
	v_med3_f32 v29, v29, s75, v180
	v_mul_f32_e32 v24, 0x41800000, v24
	v_mul_f32_e32 v25, 0x41800000, v25
	v_cvt_pk_fp8_f32 v224, v30, v29 op_sel:[0,0,1]
	v_med3_f32 v24, v24, s75, v180
	v_med3_f32 v25, v25, s75, v180
	v_pk_fma_f32 v[26:27], v[26:27], s[40:41], v[138:139] op_sel_hi:[1,0,1]
	v_cvt_pk_fp8_f32 v225, v24, v25
	v_pk_mul_f32 v[26:27], v[26:27], v[150:151] op_sel_hi:[1,0]
	v_pk_fma_f32 v[20:21], v[20:21], s[40:41], v[132:133] op_sel_hi:[1,0,1]
	v_mul_f32_e32 v26, 0x41800000, v26
	v_mul_f32_e32 v24, 0x41800000, v27
	v_pk_mul_f32 v[20:21], v[20:21], v[150:151] op_sel_hi:[1,0]
	v_med3_f32 v25, v26, s75, v180
	v_med3_f32 v24, v24, s75, v180
	v_mul_f32_e32 v20, 0x41800000, v20
	v_mul_f32_e32 v21, 0x41800000, v21
	v_cvt_pk_fp8_f32 v225, v25, v24 op_sel:[0,0,1]
	v_med3_f32 v24, v20, s75, v180
	v_med3_f32 v21, v21, s75, v180
	v_pk_fma_f32 v[22:23], v[22:23], s[40:41], v[134:135] op_sel_hi:[1,0,1]
	v_cvt_pk_fp8_f32 v226, v24, v21
	v_pk_mul_f32 v[22:23], v[22:23], v[150:151] op_sel_hi:[1,0]
	v_pk_fma_f32 v[16:17], v[16:17], s[40:41], v[128:129] op_sel_hi:[1,0,1]
	v_mul_f32_e32 v22, 0x41800000, v22
	v_pk_mul_f32 v[16:17], v[16:17], v[150:151] op_sel_hi:[1,0]
	v_mul_f32_e32 v21, 0x41800000, v23
	v_med3_f32 v22, v22, s75, v180
	v_med3_f32 v21, v21, s75, v180
	v_mul_f32_e32 v16, 0x41800000, v16
	v_mul_f32_e32 v17, 0x41800000, v17
	v_cvt_pk_fp8_f32 v226, v22, v21 op_sel:[0,0,1]
	v_med3_f32 v16, v16, s75, v180
	v_med3_f32 v17, v17, s75, v180
	v_pk_fma_f32 v[18:19], v[18:19], s[40:41], v[130:131] op_sel_hi:[1,0,1]
	v_cvt_pk_fp8_f32 v227, v16, v17
	v_pk_mul_f32 v[18:19], v[18:19], v[150:151] op_sel_hi:[1,0]
	v_lshlrev_b64 v[32:33], 11, v[144:145]
	v_mul_f32_e32 v18, 0x41800000, v18
	v_mul_f32_e32 v16, 0x41800000, v19
	v_med3_f32 v17, v18, s75, v180
	v_med3_f32 v16, v16, s75, v180
	v_cvt_pk_fp8_f32 v227, v17, v16 op_sel:[0,0,1]
	v_lshl_add_u64 v[16:17], s[36:37], 0, v[32:33]
	v_lshl_add_u64 v[16:17], v[16:17], 0, v[148:149]
	global_store_dwordx4 v[16:17], v[224:227], off
.LBB0_1271:
	s_or_b64 exec, exec, s[4:5]
	v_cndmask_b32_e32 v144, -1, v147, vcc
	v_cmp_lt_i32_e32 vcc, -1, v144
	s_and_saveexec_b64 s[0:1], vcc
	s_cbranch_execz .LBB0_1273
	v_pk_fma_f32 v[12:13], v[12:13], s[40:41], v[140:141] op_sel_hi:[1,0,1]
	v_pk_fma_f32 v[14:15], v[14:15], s[40:41], v[142:143] op_sel_hi:[1,0,1]
	v_pk_mul_f32 v[12:13], v[12:13], v[146:147] op_sel_hi:[1,0]
	v_pk_mul_f32 v[14:15], v[14:15], v[146:147] op_sel_hi:[1,0]
	v_mul_f32_e32 v12, 0x41800000, v12
	v_mul_f32_e32 v13, 0x41800000, v13
	v_med3_f32 v18, v12, s75, v180
	v_med3_f32 v13, v13, s75, v180
	v_cvt_pk_fp8_f32 v228, v18, v13
	v_pk_fma_f32 v[8:9], v[8:9], s[40:41], v[136:137] op_sel_hi:[1,0,1]
	v_mul_f32_e32 v14, 0x41800000, v14
	v_pk_mul_f32 v[8:9], v[8:9], v[146:147] op_sel_hi:[1,0]
	v_mul_f32_e32 v13, 0x41800000, v15
	v_med3_f32 v14, v14, s75, v180
	v_med3_f32 v13, v13, s75, v180
	v_mul_f32_e32 v8, 0x41800000, v8
	v_mul_f32_e32 v9, 0x41800000, v9
	v_cvt_pk_fp8_f32 v228, v14, v13 op_sel:[0,0,1]
	v_med3_f32 v8, v8, s75, v180
	v_med3_f32 v9, v9, s75, v180
	v_pk_fma_f32 v[10:11], v[10:11], s[40:41], v[138:139] op_sel_hi:[1,0,1]
	v_cvt_pk_fp8_f32 v229, v8, v9
	v_pk_mul_f32 v[10:11], v[10:11], v[146:147] op_sel_hi:[1,0]
	v_pk_fma_f32 v[4:5], v[4:5], s[40:41], v[132:133] op_sel_hi:[1,0,1]
	v_mul_f32_e32 v10, 0x41800000, v10
	v_mul_f32_e32 v8, 0x41800000, v11
	v_pk_mul_f32 v[4:5], v[4:5], v[146:147] op_sel_hi:[1,0]
	v_med3_f32 v9, v10, s75, v180
	v_med3_f32 v8, v8, s75, v180
	v_mul_f32_e32 v4, 0x41800000, v4
	v_mul_f32_e32 v5, 0x41800000, v5
	v_cvt_pk_fp8_f32 v229, v9, v8 op_sel:[0,0,1]
	v_med3_f32 v8, v4, s75, v180
	v_med3_f32 v5, v5, s75, v180
	v_pk_fma_f32 v[6:7], v[6:7], s[40:41], v[134:135] op_sel_hi:[1,0,1]
	v_cvt_pk_fp8_f32 v230, v8, v5
	v_pk_mul_f32 v[6:7], v[6:7], v[146:147] op_sel_hi:[1,0]
	v_pk_fma_f32 v[0:1], v[0:1], s[40:41], v[128:129] op_sel_hi:[1,0,1]
	v_mul_f32_e32 v6, 0x41800000, v6
	v_pk_mul_f32 v[0:1], v[0:1], v[146:147] op_sel_hi:[1,0]
	v_mul_f32_e32 v5, 0x41800000, v7
	v_med3_f32 v6, v6, s75, v180
	v_med3_f32 v5, v5, s75, v180
	v_mul_f32_e32 v0, 0x41800000, v0
	v_mul_f32_e32 v1, 0x41800000, v1
	v_cvt_pk_fp8_f32 v230, v6, v5 op_sel:[0,0,1]
	v_med3_f32 v0, v0, s75, v180
	v_med3_f32 v1, v1, s75, v180
	v_pk_fma_f32 v[2:3], v[2:3], s[40:41], v[130:131] op_sel_hi:[1,0,1]
	v_cvt_pk_fp8_f32 v231, v0, v1
	v_pk_mul_f32 v[2:3], v[2:3], v[146:147] op_sel_hi:[1,0]
	v_lshlrev_b64 v[16:17], 11, v[144:145]
	v_mul_f32_e32 v2, 0x41800000, v2
	v_mul_f32_e32 v0, 0x41800000, v3
	v_med3_f32 v1, v2, s75, v180
	v_med3_f32 v0, v0, s75, v180
	v_cvt_pk_fp8_f32 v231, v1, v0 op_sel:[0,0,1]
	v_lshl_add_u64 v[0:1], s[36:37], 0, v[16:17]
	v_lshl_add_u64 v[0:1], v[0:1], 0, v[148:149]
	global_store_dwordx4 v[0:1], v[228:231], off
